# GEMM K-loops: removed the 28 back-to-back s_setprio 0 / s_setprio 1 pairs in the middle of each MMA phase (outer raise/lower kept)
# speedup vs baseline: 1.0036x; 1.0010x over previous
.LBB0_48:
	s_ashr_i32 s51, s50, 31
	s_lshl_b64 s[58:59], s[50:51], 18
	s_add_u32 s58, s14, s58
	s_addc_u32 s59, s15, s59
	s_and_b64 s[60:61], s[54:55], exec
	s_cselect_b32 s6, s59, s27
	s_cselect_b32 s51, s58, s26
	s_ashr_i32 s53, s52, 31
	s_lshl_b64 s[60:61], s[52:53], 20
	s_add_u32 s4, s16, s60
	s_addc_u32 s53, s17, s61
	s_ashr_i32 s49, s48, 31
	s_lshl_b64 s[60:61], s[48:49], 18
	s_add_u32 s60, s4, s60
	s_addc_u32 s61, s53, s61
	s_and_b64 s[68:69], s[54:55], exec
	s_cselect_b32 s49, s61, s37
	s_cselect_b32 s53, s60, s36
	s_add_u32 s26, s26, 0x20080
	s_addc_u32 s27, s27, 0
	s_add_u32 s65, s36, 0x100
	s_addc_u32 s74, s37, 0
	s_mov_b32 s92, -2
	s_add_u32 s36, s26, 0xfffe0080
	s_addc_u32 s37, s27, -1
	s_add_i32 s4, 0, 0x10000
	s_cmp_eq_u32 s92, 4
	s_cselect_b32 s69, s6, s37
	s_cselect_b32 s68, s51, s36
	s_cselect_b32 s37, s49, s74
	s_cselect_b32 s36, s53, s65
	s_add_i32 s93, 0, 0x14000
	v_add_u32_e32 v2, s4, v184
	v_add_u32_e32 v14, s93, v184
	ds_read_b128 v[18:21], v2
	ds_read_b128 v[22:25], v2 offset:1024
	ds_read_b128 v[26:29], v2 offset:2048
	ds_read_b128 v[30:33], v2 offset:3072
	ds_read_b128 v[2:5], v14
	ds_read_b128 v[6:9], v14 offset:1024
	ds_read_b128 v[10:13], v14 offset:2048
	ds_read_b128 v[14:17], v14 offset:3072
	v_lshl_add_u64 v[188:189], s[26:27], 0, v[170:171]
	s_add_i32 m0, s63, 0xc000
	ds_read_b128 v[174:177], v187
	ds_read_b128 v[178:181], v187 offset:1024
	ds_read_b128 v[196:199], v187 offset:2048
	ds_read_b128 v[200:203], v187 offset:3072
	ds_read_b128 v[204:207], v187 offset:4096
	ds_read_b128 v[208:211], v187 offset:5120
	ds_read_b128 v[212:215], v187 offset:6144
	ds_read_b128 v[216:219], v187 offset:7168
	global_load_lds_dwordx4 v[188:189], off
	v_lshl_add_u64 v[188:189], s[26:27], 0, v[172:173]
	s_add_i32 m0, s63, 0xe000
	s_nop 0
	global_load_lds_dwordx4 v[188:189], off
	s_waitcnt vmcnt(8)
	s_waitcnt lgkmcnt(0)
	s_barrier
	s_setprio 1
	s_waitcnt lgkmcnt(0)
	v_mfma_scale_f32_16x16x128_f8f6f4 v[158:161], v[18:25], v[174:181], 0, v191, v191 op_sel_hi:[0,0,0]
	v_mfma_scale_f32_16x16x128_f8f6f4 v[154:157], v[26:33], v[174:181], 0, v191, v191 op_sel_hi:[0,0,0]
	v_mfma_scale_f32_16x16x128_f8f6f4 v[150:153], v[18:25], v[196:203], 0, v191, v191 op_sel_hi:[0,0,0]
	v_mfma_scale_f32_16x16x128_f8f6f4 v[146:149], v[26:33], v[196:203], 0, v191, v191 op_sel_hi:[0,0,0]
	v_mfma_scale_f32_16x16x128_f8f6f4 v[126:129], v[18:25], v[204:211], 0, v191, v191 op_sel_hi:[0,0,0]
	v_mfma_scale_f32_16x16x128_f8f6f4 v[122:125], v[26:33], v[204:211], 0, v191, v191 op_sel_hi:[0,0,0]
	v_mfma_scale_f32_16x16x128_f8f6f4 v[118:121], v[18:25], v[212:219], 0, v191, v191 op_sel_hi:[0,0,0]
	v_mfma_scale_f32_16x16x128_f8f6f4 v[114:117], v[26:33], v[212:219], 0, v191, v191 op_sel_hi:[0,0,0]
	v_mfma_scale_f32_16x16x128_f8f6f4 v[142:145], v[2:9], v[174:181], 0, v191, v191 op_sel_hi:[0,0,0]
	v_mfma_scale_f32_16x16x128_f8f6f4 v[138:141], v[10:17], v[174:181], 0, v191, v191 op_sel_hi:[0,0,0]
	v_mfma_scale_f32_16x16x128_f8f6f4 v[134:137], v[2:9], v[196:203], 0, v191, v191 op_sel_hi:[0,0,0]
	v_mfma_scale_f32_16x16x128_f8f6f4 v[130:133], v[10:17], v[196:203], 0, v191, v191 op_sel_hi:[0,0,0]
	v_mfma_scale_f32_16x16x128_f8f6f4 v[110:113], v[2:9], v[204:211], 0, v191, v191 op_sel_hi:[0,0,0]
	v_mfma_scale_f32_16x16x128_f8f6f4 v[106:109], v[10:17], v[204:211], 0, v191, v191 op_sel_hi:[0,0,0]
	v_mfma_scale_f32_16x16x128_f8f6f4 v[102:105], v[2:9], v[212:219], 0, v191, v191 op_sel_hi:[0,0,0]
	v_mfma_scale_f32_16x16x128_f8f6f4 v[98:101], v[10:17], v[212:219], 0, v191, v191 op_sel_hi:[0,0,0]
	s_setprio 0
	s_barrier
	s_add_i32 s4, s4, s45
	v_lshl_add_u64 v[174:175], s[36:37], 0, v[0:1]
	s_mov_b32 m0, s4
	ds_read_b128 v[196:199], v187 offset:16384
	ds_read_b128 v[200:203], v187 offset:17408
	ds_read_b128 v[204:207], v187 offset:18432
	ds_read_b128 v[208:211], v187 offset:19456
	ds_read_b128 v[212:215], v187 offset:20480
	ds_read_b128 v[216:219], v187 offset:21504
	ds_read_b128 v[234:237], v187 offset:22528
	ds_read_b128 v[238:241], v187 offset:23552
	global_load_lds_dwordx4 v[174:175], off
	s_add_i32 m0, s4, 0x2000
	s_add_u32 s86, s36, 0x20000
	v_lshl_add_u64 v[176:177], s[36:37], 0, v[166:167]
	s_addc_u32 s87, s37, 0
	s_add_i32 s4, s93, s45
	global_load_lds_dwordx4 v[176:177], off
	v_lshl_add_u64 v[178:179], s[86:87], 0, v[0:1]
	s_mov_b32 m0, s4
	v_lshl_add_u64 v[180:181], s[68:69], 0, v[164:165]
	global_load_lds_dwordx4 v[178:179], off
	v_lshl_add_u64 v[178:179], s[86:87], 0, v[166:167]
	s_add_i32 m0, s4, 0x2000
	s_nop 0
	global_load_lds_dwordx4 v[178:179], off
	v_lshl_add_u64 v[178:179], s[68:69], 0, v[162:163]
	s_mov_b32 m0, s63
	s_nop 0
	global_load_lds_dwordx4 v[178:179], off
	s_mov_b32 m0, s67
	s_nop 0
	global_load_lds_dwordx4 v[180:181], off
	s_waitcnt vmcnt(8)
	s_waitcnt lgkmcnt(0)
	s_barrier
	s_setprio 1
	s_waitcnt lgkmcnt(0)
	v_mfma_scale_f32_16x16x128_f8f6f4 v[94:97], v[18:25], v[196:203], 0, v191, v191 op_sel_hi:[0,0,0]
	v_mfma_scale_f32_16x16x128_f8f6f4 v[90:93], v[26:33], v[196:203], 0, v191, v191 op_sel_hi:[0,0,0]
	v_mfma_scale_f32_16x16x128_f8f6f4 v[86:89], v[18:25], v[204:211], 0, v191, v191 op_sel_hi:[0,0,0]
	v_mfma_scale_f32_16x16x128_f8f6f4 v[82:85], v[26:33], v[204:211], 0, v191, v191 op_sel_hi:[0,0,0]
	v_mfma_scale_f32_16x16x128_f8f6f4 v[62:65], v[18:25], v[212:219], 0, v191, v191 op_sel_hi:[0,0,0]
	v_mfma_scale_f32_16x16x128_f8f6f4 v[58:61], v[26:33], v[212:219], 0, v191, v191 op_sel_hi:[0,0,0]
	v_mfma_scale_f32_16x16x128_f8f6f4 v[54:57], v[18:25], v[234:241], 0, v191, v191 op_sel_hi:[0,0,0]
	v_mfma_scale_f32_16x16x128_f8f6f4 v[50:53], v[26:33], v[234:241], 0, v191, v191 op_sel_hi:[0,0,0]
	v_mfma_scale_f32_16x16x128_f8f6f4 v[78:81], v[2:9], v[196:203], 0, v191, v191 op_sel_hi:[0,0,0]
	v_mfma_scale_f32_16x16x128_f8f6f4 v[74:77], v[10:17], v[196:203], 0, v191, v191 op_sel_hi:[0,0,0]
	v_mfma_scale_f32_16x16x128_f8f6f4 v[70:73], v[2:9], v[204:211], 0, v191, v191 op_sel_hi:[0,0,0]
	v_mfma_scale_f32_16x16x128_f8f6f4 v[66:69], v[10:17], v[204:211], 0, v191, v191 op_sel_hi:[0,0,0]
	v_mfma_scale_f32_16x16x128_f8f6f4 v[46:49], v[2:9], v[212:219], 0, v191, v191 op_sel_hi:[0,0,0]
	v_mfma_scale_f32_16x16x128_f8f6f4 v[42:45], v[10:17], v[212:219], 0, v191, v191 op_sel_hi:[0,0,0]
	v_mfma_scale_f32_16x16x128_f8f6f4 v[38:41], v[2:9], v[234:241], 0, v191, v191 op_sel_hi:[0,0,0]
	v_mfma_scale_f32_16x16x128_f8f6f4 v[34:37], v[10:17], v[234:241], 0, v191, v191 op_sel_hi:[0,0,0]
	s_setprio 0
	s_barrier
	s_add_i32 s4, 0, 0x18000
	s_add_i32 s86, 0, 0x1c000
	v_add_u32_e32 v14, s4, v184
	v_add_u32_e32 v30, s86, v184
	ds_read_b128 v[2:5], v14
	ds_read_b128 v[6:9], v14 offset:1024
	ds_read_b128 v[10:13], v14 offset:2048
	ds_read_b128 v[14:17], v14 offset:3072
	ds_read_b128 v[18:21], v30
	ds_read_b128 v[22:25], v30 offset:1024
	ds_read_b128 v[26:29], v30 offset:2048
	ds_read_b128 v[30:33], v30 offset:3072
	s_add_u32 s68, s68, 0x20000
	s_addc_u32 s69, s69, 0
	s_mov_b32 m0, s73
	v_lshl_add_u64 v[188:189], s[68:69], 0, v[162:163]
	ds_read_b128 v[196:199], v187 offset:32768
	ds_read_b128 v[200:203], v187 offset:33792
	ds_read_b128 v[204:207], v187 offset:34816
	ds_read_b128 v[208:211], v187 offset:35840
	ds_read_b128 v[212:215], v187 offset:36864
	ds_read_b128 v[216:219], v187 offset:37888
	ds_read_b128 v[234:237], v187 offset:38912
	ds_read_b128 v[238:241], v187 offset:39936
	global_load_lds_dwordx4 v[188:189], off
	v_lshl_add_u64 v[188:189], s[68:69], 0, v[164:165]
	s_mov_b32 m0, s75
	s_nop 0
	global_load_lds_dwordx4 v[188:189], off
	s_waitcnt vmcnt(8)
	s_waitcnt lgkmcnt(0)
	s_barrier
	s_setprio 1
	s_waitcnt lgkmcnt(0)
	v_mfma_scale_f32_16x16x128_f8f6f4 v[158:161], v[2:9], v[196:203], v[158:161], v191, v191 op_sel_hi:[0,0,0]
	v_mfma_scale_f32_16x16x128_f8f6f4 v[154:157], v[10:17], v[196:203], v[154:157], v191, v191 op_sel_hi:[0,0,0]
	v_mfma_scale_f32_16x16x128_f8f6f4 v[150:153], v[2:9], v[204:211], v[150:153], v191, v191 op_sel_hi:[0,0,0]
	v_mfma_scale_f32_16x16x128_f8f6f4 v[146:149], v[10:17], v[204:211], v[146:149], v191, v191 op_sel_hi:[0,0,0]
	v_mfma_scale_f32_16x16x128_f8f6f4 v[126:129], v[2:9], v[212:219], v[126:129], v191, v191 op_sel_hi:[0,0,0]
	v_mfma_scale_f32_16x16x128_f8f6f4 v[122:125], v[10:17], v[212:219], v[122:125], v191, v191 op_sel_hi:[0,0,0]
	v_mfma_scale_f32_16x16x128_f8f6f4 v[118:121], v[2:9], v[234:241], v[118:121], v191, v191 op_sel_hi:[0,0,0]
	v_mfma_scale_f32_16x16x128_f8f6f4 v[114:117], v[10:17], v[234:241], v[114:117], v191, v191 op_sel_hi:[0,0,0]
	v_mfma_scale_f32_16x16x128_f8f6f4 v[142:145], v[18:25], v[196:203], v[142:145], v191, v191 op_sel_hi:[0,0,0]
	v_mfma_scale_f32_16x16x128_f8f6f4 v[138:141], v[26:33], v[196:203], v[138:141], v191, v191 op_sel_hi:[0,0,0]
	v_mfma_scale_f32_16x16x128_f8f6f4 v[134:137], v[18:25], v[204:211], v[134:137], v191, v191 op_sel_hi:[0,0,0]
	v_mfma_scale_f32_16x16x128_f8f6f4 v[130:133], v[26:33], v[204:211], v[130:133], v191, v191 op_sel_hi:[0,0,0]
	v_mfma_scale_f32_16x16x128_f8f6f4 v[110:113], v[18:25], v[212:219], v[110:113], v191, v191 op_sel_hi:[0,0,0]
	v_mfma_scale_f32_16x16x128_f8f6f4 v[106:109], v[26:33], v[212:219], v[106:109], v191, v191 op_sel_hi:[0,0,0]
	v_mfma_scale_f32_16x16x128_f8f6f4 v[102:105], v[18:25], v[234:241], v[102:105], v191, v191 op_sel_hi:[0,0,0]
	v_mfma_scale_f32_16x16x128_f8f6f4 v[98:101], v[26:33], v[234:241], v[98:101], v191, v191 op_sel_hi:[0,0,0]
	s_setprio 0
	s_barrier
	s_add_i32 s4, s4, s45
	v_lshl_add_u64 v[174:175], v[174:175], 0, s[22:23]
	s_mov_b32 m0, s4
	ds_read_b128 v[196:199], v187 offset:49152
	ds_read_b128 v[200:203], v187 offset:50176
	ds_read_b128 v[204:207], v187 offset:51200
	ds_read_b128 v[208:211], v187 offset:52224
	ds_read_b128 v[212:215], v187 offset:53248
	ds_read_b128 v[216:219], v187 offset:54272
	ds_read_b128 v[234:237], v187 offset:55296
	ds_read_b128 v[238:241], v187 offset:56320
	global_load_lds_dwordx4 v[174:175], off
	s_add_i32 m0, s4, 0x2000
	s_add_u32 s36, s36, 0x20080
	v_lshl_add_u64 v[174:175], v[176:177], 0, s[22:23]
	s_addc_u32 s37, s37, 0
	s_add_i32 s4, s86, s45
	global_load_lds_dwordx4 v[174:175], off
	v_lshl_add_u64 v[174:175], s[36:37], 0, v[0:1]
	s_mov_b32 m0, s4
	s_nop 0
	global_load_lds_dwordx4 v[174:175], off
	v_lshl_add_u64 v[174:175], s[36:37], 0, v[166:167]
	s_add_i32 m0, s4, 0x2000
	s_nop 0
	global_load_lds_dwordx4 v[174:175], off
	v_lshl_add_u64 v[174:175], v[178:179], 0, s[22:23]
	s_mov_b32 m0, s79
	s_nop 0
	global_load_lds_dwordx4 v[174:175], off
	v_lshl_add_u64 v[174:175], v[180:181], 0, s[22:23]
	s_mov_b32 m0, s82
	s_nop 0
	global_load_lds_dwordx4 v[174:175], off
	s_waitcnt vmcnt(8)
	s_waitcnt lgkmcnt(0)
	s_barrier
	s_setprio 1
	s_waitcnt lgkmcnt(0)
	v_mfma_scale_f32_16x16x128_f8f6f4 v[94:97], v[2:9], v[196:203], v[94:97], v191, v191 op_sel_hi:[0,0,0]
	v_mfma_scale_f32_16x16x128_f8f6f4 v[90:93], v[10:17], v[196:203], v[90:93], v191, v191 op_sel_hi:[0,0,0]
	v_mfma_scale_f32_16x16x128_f8f6f4 v[86:89], v[2:9], v[204:211], v[86:89], v191, v191 op_sel_hi:[0,0,0]
	v_mfma_scale_f32_16x16x128_f8f6f4 v[82:85], v[10:17], v[204:211], v[82:85], v191, v191 op_sel_hi:[0,0,0]
	v_mfma_scale_f32_16x16x128_f8f6f4 v[62:65], v[2:9], v[212:219], v[62:65], v191, v191 op_sel_hi:[0,0,0]
	v_mfma_scale_f32_16x16x128_f8f6f4 v[58:61], v[10:17], v[212:219], v[58:61], v191, v191 op_sel_hi:[0,0,0]
	v_mfma_scale_f32_16x16x128_f8f6f4 v[54:57], v[2:9], v[234:241], v[54:57], v191, v191 op_sel_hi:[0,0,0]
	v_mfma_scale_f32_16x16x128_f8f6f4 v[50:53], v[10:17], v[234:241], v[50:53], v191, v191 op_sel_hi:[0,0,0]
	v_mfma_scale_f32_16x16x128_f8f6f4 v[78:81], v[18:25], v[196:203], v[78:81], v191, v191 op_sel_hi:[0,0,0]
	v_mfma_scale_f32_16x16x128_f8f6f4 v[74:77], v[26:33], v[196:203], v[74:77], v191, v191 op_sel_hi:[0,0,0]
	v_mfma_scale_f32_16x16x128_f8f6f4 v[70:73], v[18:25], v[204:211], v[70:73], v191, v191 op_sel_hi:[0,0,0]
	v_mfma_scale_f32_16x16x128_f8f6f4 v[66:69], v[26:33], v[204:211], v[66:69], v191, v191 op_sel_hi:[0,0,0]
	v_mfma_scale_f32_16x16x128_f8f6f4 v[46:49], v[18:25], v[212:219], v[46:49], v191, v191 op_sel_hi:[0,0,0]
	v_mfma_scale_f32_16x16x128_f8f6f4 v[42:45], v[26:33], v[212:219], v[42:45], v191, v191 op_sel_hi:[0,0,0]
	v_mfma_scale_f32_16x16x128_f8f6f4 v[38:41], v[18:25], v[234:241], v[38:41], v191, v191 op_sel_hi:[0,0,0]
	v_mfma_scale_f32_16x16x128_f8f6f4 v[34:37], v[26:33], v[234:241], v[34:37], v191, v191 op_sel_hi:[0,0,0]
	s_setprio 0
	s_barrier
	s_add_i32 s92, s92, 2
	s_add_u32 s26, s26, 0x100
	s_addc_u32 s27, s27, 0
	s_add_u32 s65, s65, 0x100
	s_addc_u32 s74, s74, 0
.LBB0_49:
	s_add_u32 s36, s26, 0xfffe0080
	s_addc_u32 s37, s27, -1
	s_add_i32 s4, 0, 0x10000
	s_cmp_eq_u32 s92, 4
	s_cselect_b32 s69, s6, s37
	s_cselect_b32 s68, s51, s36
	s_cselect_b32 s37, s49, s74
	s_cselect_b32 s36, s53, s65
	s_add_i32 s93, 0, 0x14000
	v_add_u32_e32 v2, s4, v184
	v_add_u32_e32 v14, s93, v184
	ds_read_b128 v[18:21], v2
	ds_read_b128 v[22:25], v2 offset:1024
	ds_read_b128 v[26:29], v2 offset:2048
	ds_read_b128 v[30:33], v2 offset:3072
	ds_read_b128 v[2:5], v14
	ds_read_b128 v[6:9], v14 offset:1024
	ds_read_b128 v[10:13], v14 offset:2048
	ds_read_b128 v[14:17], v14 offset:3072
	v_lshl_add_u64 v[188:189], s[26:27], 0, v[170:171]
	s_add_i32 m0, s63, 0xc000
	ds_read_b128 v[174:177], v187
	ds_read_b128 v[178:181], v187 offset:1024
	ds_read_b128 v[196:199], v187 offset:2048
	ds_read_b128 v[200:203], v187 offset:3072
	ds_read_b128 v[204:207], v187 offset:4096
	ds_read_b128 v[208:211], v187 offset:5120
	ds_read_b128 v[212:215], v187 offset:6144
	ds_read_b128 v[216:219], v187 offset:7168
	global_load_lds_dwordx4 v[188:189], off
	v_lshl_add_u64 v[188:189], s[26:27], 0, v[172:173]
	s_add_i32 m0, s63, 0xe000
	s_nop 0
	global_load_lds_dwordx4 v[188:189], off
	s_waitcnt vmcnt(8)
	s_waitcnt lgkmcnt(0)
	s_barrier
	s_setprio 1
	s_waitcnt lgkmcnt(0)
	v_mfma_scale_f32_16x16x128_f8f6f4 v[158:161], v[18:25], v[174:181], v[158:161], v191, v191 op_sel_hi:[0,0,0]
	v_mfma_scale_f32_16x16x128_f8f6f4 v[154:157], v[26:33], v[174:181], v[154:157], v191, v191 op_sel_hi:[0,0,0]
	v_mfma_scale_f32_16x16x128_f8f6f4 v[150:153], v[18:25], v[196:203], v[150:153], v191, v191 op_sel_hi:[0,0,0]
	v_mfma_scale_f32_16x16x128_f8f6f4 v[146:149], v[26:33], v[196:203], v[146:149], v191, v191 op_sel_hi:[0,0,0]
	v_mfma_scale_f32_16x16x128_f8f6f4 v[126:129], v[18:25], v[204:211], v[126:129], v191, v191 op_sel_hi:[0,0,0]
	v_mfma_scale_f32_16x16x128_f8f6f4 v[122:125], v[26:33], v[204:211], v[122:125], v191, v191 op_sel_hi:[0,0,0]
	v_mfma_scale_f32_16x16x128_f8f6f4 v[118:121], v[18:25], v[212:219], v[118:121], v191, v191 op_sel_hi:[0,0,0]
	v_mfma_scale_f32_16x16x128_f8f6f4 v[114:117], v[26:33], v[212:219], v[114:117], v191, v191 op_sel_hi:[0,0,0]
	v_mfma_scale_f32_16x16x128_f8f6f4 v[142:145], v[2:9], v[174:181], v[142:145], v191, v191 op_sel_hi:[0,0,0]
	v_mfma_scale_f32_16x16x128_f8f6f4 v[138:141], v[10:17], v[174:181], v[138:141], v191, v191 op_sel_hi:[0,0,0]
	v_mfma_scale_f32_16x16x128_f8f6f4 v[134:137], v[2:9], v[196:203], v[134:137], v191, v191 op_sel_hi:[0,0,0]
	v_mfma_scale_f32_16x16x128_f8f6f4 v[130:133], v[10:17], v[196:203], v[130:133], v191, v191 op_sel_hi:[0,0,0]
	v_mfma_scale_f32_16x16x128_f8f6f4 v[110:113], v[2:9], v[204:211], v[110:113], v191, v191 op_sel_hi:[0,0,0]
	v_mfma_scale_f32_16x16x128_f8f6f4 v[106:109], v[10:17], v[204:211], v[106:109], v191, v191 op_sel_hi:[0,0,0]
	v_mfma_scale_f32_16x16x128_f8f6f4 v[102:105], v[2:9], v[212:219], v[102:105], v191, v191 op_sel_hi:[0,0,0]
	v_mfma_scale_f32_16x16x128_f8f6f4 v[98:101], v[10:17], v[212:219], v[98:101], v191, v191 op_sel_hi:[0,0,0]
	s_setprio 0
	s_barrier
	s_add_i32 s4, s4, s45
	v_lshl_add_u64 v[174:175], s[36:37], 0, v[0:1]
	s_mov_b32 m0, s4
	ds_read_b128 v[196:199], v187 offset:16384
	ds_read_b128 v[200:203], v187 offset:17408
	ds_read_b128 v[204:207], v187 offset:18432
	ds_read_b128 v[208:211], v187 offset:19456
	ds_read_b128 v[212:215], v187 offset:20480
	ds_read_b128 v[216:219], v187 offset:21504
	ds_read_b128 v[234:237], v187 offset:22528
	ds_read_b128 v[238:241], v187 offset:23552
	global_load_lds_dwordx4 v[174:175], off
	s_add_i32 m0, s4, 0x2000
	s_add_u32 s86, s36, 0x20000
	v_lshl_add_u64 v[176:177], s[36:37], 0, v[166:167]
	s_addc_u32 s87, s37, 0
	s_add_i32 s4, s93, s45
	global_load_lds_dwordx4 v[176:177], off
	v_lshl_add_u64 v[178:179], s[86:87], 0, v[0:1]
	s_mov_b32 m0, s4
	v_lshl_add_u64 v[180:181], s[68:69], 0, v[164:165]
	global_load_lds_dwordx4 v[178:179], off
	v_lshl_add_u64 v[178:179], s[86:87], 0, v[166:167]
	s_add_i32 m0, s4, 0x2000
	s_nop 0
	global_load_lds_dwordx4 v[178:179], off
	v_lshl_add_u64 v[178:179], s[68:69], 0, v[162:163]
	s_mov_b32 m0, s63
	s_nop 0
	global_load_lds_dwordx4 v[178:179], off
	s_mov_b32 m0, s67
	s_nop 0
	global_load_lds_dwordx4 v[180:181], off
	s_waitcnt vmcnt(8)
	s_waitcnt lgkmcnt(0)
	s_barrier
	s_setprio 1
	s_waitcnt lgkmcnt(0)
	v_mfma_scale_f32_16x16x128_f8f6f4 v[94:97], v[18:25], v[196:203], v[94:97], v191, v191 op_sel_hi:[0,0,0]
	v_mfma_scale_f32_16x16x128_f8f6f4 v[90:93], v[26:33], v[196:203], v[90:93], v191, v191 op_sel_hi:[0,0,0]
	v_mfma_scale_f32_16x16x128_f8f6f4 v[86:89], v[18:25], v[204:211], v[86:89], v191, v191 op_sel_hi:[0,0,0]
	v_mfma_scale_f32_16x16x128_f8f6f4 v[82:85], v[26:33], v[204:211], v[82:85], v191, v191 op_sel_hi:[0,0,0]
	v_mfma_scale_f32_16x16x128_f8f6f4 v[62:65], v[18:25], v[212:219], v[62:65], v191, v191 op_sel_hi:[0,0,0]
	v_mfma_scale_f32_16x16x128_f8f6f4 v[58:61], v[26:33], v[212:219], v[58:61], v191, v191 op_sel_hi:[0,0,0]
	v_mfma_scale_f32_16x16x128_f8f6f4 v[54:57], v[18:25], v[234:241], v[54:57], v191, v191 op_sel_hi:[0,0,0]
	v_mfma_scale_f32_16x16x128_f8f6f4 v[50:53], v[26:33], v[234:241], v[50:53], v191, v191 op_sel_hi:[0,0,0]
	v_mfma_scale_f32_16x16x128_f8f6f4 v[78:81], v[2:9], v[196:203], v[78:81], v191, v191 op_sel_hi:[0,0,0]
	v_mfma_scale_f32_16x16x128_f8f6f4 v[74:77], v[10:17], v[196:203], v[74:77], v191, v191 op_sel_hi:[0,0,0]
	v_mfma_scale_f32_16x16x128_f8f6f4 v[70:73], v[2:9], v[204:211], v[70:73], v191, v191 op_sel_hi:[0,0,0]
	v_mfma_scale_f32_16x16x128_f8f6f4 v[66:69], v[10:17], v[204:211], v[66:69], v191, v191 op_sel_hi:[0,0,0]
	v_mfma_scale_f32_16x16x128_f8f6f4 v[46:49], v[2:9], v[212:219], v[46:49], v191, v191 op_sel_hi:[0,0,0]
	v_mfma_scale_f32_16x16x128_f8f6f4 v[42:45], v[10:17], v[212:219], v[42:45], v191, v191 op_sel_hi:[0,0,0]
	v_mfma_scale_f32_16x16x128_f8f6f4 v[38:41], v[2:9], v[234:241], v[38:41], v191, v191 op_sel_hi:[0,0,0]
	v_mfma_scale_f32_16x16x128_f8f6f4 v[34:37], v[10:17], v[234:241], v[34:37], v191, v191 op_sel_hi:[0,0,0]
	s_setprio 0
	s_barrier
	s_add_i32 s4, 0, 0x18000
	s_add_i32 s86, 0, 0x1c000
	v_add_u32_e32 v14, s4, v184
	v_add_u32_e32 v30, s86, v184
	ds_read_b128 v[2:5], v14
	ds_read_b128 v[6:9], v14 offset:1024
	ds_read_b128 v[10:13], v14 offset:2048
	ds_read_b128 v[14:17], v14 offset:3072
	ds_read_b128 v[18:21], v30
	ds_read_b128 v[22:25], v30 offset:1024
	ds_read_b128 v[26:29], v30 offset:2048
	ds_read_b128 v[30:33], v30 offset:3072
	s_add_u32 s68, s68, 0x20000
	s_addc_u32 s69, s69, 0
	s_mov_b32 m0, s73
	v_lshl_add_u64 v[188:189], s[68:69], 0, v[162:163]
	ds_read_b128 v[196:199], v187 offset:32768
	ds_read_b128 v[200:203], v187 offset:33792
	ds_read_b128 v[204:207], v187 offset:34816
	ds_read_b128 v[208:211], v187 offset:35840
	ds_read_b128 v[212:215], v187 offset:36864
	ds_read_b128 v[216:219], v187 offset:37888
	ds_read_b128 v[234:237], v187 offset:38912
	ds_read_b128 v[238:241], v187 offset:39936
	global_load_lds_dwordx4 v[188:189], off
	v_lshl_add_u64 v[188:189], s[68:69], 0, v[164:165]
	s_mov_b32 m0, s75
	s_nop 0
	global_load_lds_dwordx4 v[188:189], off
	s_waitcnt vmcnt(8)
	s_waitcnt lgkmcnt(0)
	s_barrier
	s_setprio 1
	s_waitcnt lgkmcnt(0)
	v_mfma_scale_f32_16x16x128_f8f6f4 v[158:161], v[2:9], v[196:203], v[158:161], v191, v191 op_sel_hi:[0,0,0]
	v_mfma_scale_f32_16x16x128_f8f6f4 v[154:157], v[10:17], v[196:203], v[154:157], v191, v191 op_sel_hi:[0,0,0]
	v_mfma_scale_f32_16x16x128_f8f6f4 v[150:153], v[2:9], v[204:211], v[150:153], v191, v191 op_sel_hi:[0,0,0]
	v_mfma_scale_f32_16x16x128_f8f6f4 v[146:149], v[10:17], v[204:211], v[146:149], v191, v191 op_sel_hi:[0,0,0]
	v_mfma_scale_f32_16x16x128_f8f6f4 v[126:129], v[2:9], v[212:219], v[126:129], v191, v191 op_sel_hi:[0,0,0]
	v_mfma_scale_f32_16x16x128_f8f6f4 v[122:125], v[10:17], v[212:219], v[122:125], v191, v191 op_sel_hi:[0,0,0]
	v_mfma_scale_f32_16x16x128_f8f6f4 v[118:121], v[2:9], v[234:241], v[118:121], v191, v191 op_sel_hi:[0,0,0]
	v_mfma_scale_f32_16x16x128_f8f6f4 v[114:117], v[10:17], v[234:241], v[114:117], v191, v191 op_sel_hi:[0,0,0]
	v_mfma_scale_f32_16x16x128_f8f6f4 v[142:145], v[18:25], v[196:203], v[142:145], v191, v191 op_sel_hi:[0,0,0]
	v_mfma_scale_f32_16x16x128_f8f6f4 v[138:141], v[26:33], v[196:203], v[138:141], v191, v191 op_sel_hi:[0,0,0]
	v_mfma_scale_f32_16x16x128_f8f6f4 v[134:137], v[18:25], v[204:211], v[134:137], v191, v191 op_sel_hi:[0,0,0]
	v_mfma_scale_f32_16x16x128_f8f6f4 v[130:133], v[26:33], v[204:211], v[130:133], v191, v191 op_sel_hi:[0,0,0]
	v_mfma_scale_f32_16x16x128_f8f6f4 v[110:113], v[18:25], v[212:219], v[110:113], v191, v191 op_sel_hi:[0,0,0]
	v_mfma_scale_f32_16x16x128_f8f6f4 v[106:109], v[26:33], v[212:219], v[106:109], v191, v191 op_sel_hi:[0,0,0]
	v_mfma_scale_f32_16x16x128_f8f6f4 v[102:105], v[18:25], v[234:241], v[102:105], v191, v191 op_sel_hi:[0,0,0]
	v_mfma_scale_f32_16x16x128_f8f6f4 v[98:101], v[26:33], v[234:241], v[98:101], v191, v191 op_sel_hi:[0,0,0]
	s_setprio 0
	s_barrier
	s_add_i32 s4, s4, s45
	v_lshl_add_u64 v[174:175], v[174:175], 0, s[22:23]
	s_mov_b32 m0, s4
	ds_read_b128 v[196:199], v187 offset:49152
	ds_read_b128 v[200:203], v187 offset:50176
	ds_read_b128 v[204:207], v187 offset:51200
	ds_read_b128 v[208:211], v187 offset:52224
	ds_read_b128 v[212:215], v187 offset:53248
	ds_read_b128 v[216:219], v187 offset:54272
	ds_read_b128 v[234:237], v187 offset:55296
	ds_read_b128 v[238:241], v187 offset:56320
	global_load_lds_dwordx4 v[174:175], off
	s_add_i32 m0, s4, 0x2000
	s_add_u32 s36, s36, 0x20080
	v_lshl_add_u64 v[174:175], v[176:177], 0, s[22:23]
	s_addc_u32 s37, s37, 0
	s_add_i32 s4, s86, s45
	global_load_lds_dwordx4 v[174:175], off
	v_lshl_add_u64 v[174:175], s[36:37], 0, v[0:1]
	s_mov_b32 m0, s4
	s_nop 0
	global_load_lds_dwordx4 v[174:175], off
	v_lshl_add_u64 v[174:175], s[36:37], 0, v[166:167]
	s_add_i32 m0, s4, 0x2000
	s_nop 0
	global_load_lds_dwordx4 v[174:175], off
	v_lshl_add_u64 v[174:175], v[178:179], 0, s[22:23]
	s_mov_b32 m0, s79
	s_nop 0
	global_load_lds_dwordx4 v[174:175], off
	v_lshl_add_u64 v[174:175], v[180:181], 0, s[22:23]
	s_mov_b32 m0, s82
	s_nop 0
	global_load_lds_dwordx4 v[174:175], off
	s_waitcnt vmcnt(8)
	s_waitcnt lgkmcnt(0)
	s_barrier
	s_setprio 1
	s_waitcnt lgkmcnt(0)
	v_mfma_scale_f32_16x16x128_f8f6f4 v[94:97], v[2:9], v[196:203], v[94:97], v191, v191 op_sel_hi:[0,0,0]
	v_mfma_scale_f32_16x16x128_f8f6f4 v[90:93], v[10:17], v[196:203], v[90:93], v191, v191 op_sel_hi:[0,0,0]
	v_mfma_scale_f32_16x16x128_f8f6f4 v[86:89], v[2:9], v[204:211], v[86:89], v191, v191 op_sel_hi:[0,0,0]
	v_mfma_scale_f32_16x16x128_f8f6f4 v[82:85], v[10:17], v[204:211], v[82:85], v191, v191 op_sel_hi:[0,0,0]
	v_mfma_scale_f32_16x16x128_f8f6f4 v[62:65], v[2:9], v[212:219], v[62:65], v191, v191 op_sel_hi:[0,0,0]
	v_mfma_scale_f32_16x16x128_f8f6f4 v[58:61], v[10:17], v[212:219], v[58:61], v191, v191 op_sel_hi:[0,0,0]
	v_mfma_scale_f32_16x16x128_f8f6f4 v[54:57], v[2:9], v[234:241], v[54:57], v191, v191 op_sel_hi:[0,0,0]
	v_mfma_scale_f32_16x16x128_f8f6f4 v[50:53], v[10:17], v[234:241], v[50:53], v191, v191 op_sel_hi:[0,0,0]
	v_mfma_scale_f32_16x16x128_f8f6f4 v[78:81], v[18:25], v[196:203], v[78:81], v191, v191 op_sel_hi:[0,0,0]
	v_mfma_scale_f32_16x16x128_f8f6f4 v[74:77], v[26:33], v[196:203], v[74:77], v191, v191 op_sel_hi:[0,0,0]
	v_mfma_scale_f32_16x16x128_f8f6f4 v[70:73], v[18:25], v[204:211], v[70:73], v191, v191 op_sel_hi:[0,0,0]
	v_mfma_scale_f32_16x16x128_f8f6f4 v[66:69], v[26:33], v[204:211], v[66:69], v191, v191 op_sel_hi:[0,0,0]
	v_mfma_scale_f32_16x16x128_f8f6f4 v[46:49], v[18:25], v[212:219], v[46:49], v191, v191 op_sel_hi:[0,0,0]
	v_mfma_scale_f32_16x16x128_f8f6f4 v[42:45], v[26:33], v[212:219], v[42:45], v191, v191 op_sel_hi:[0,0,0]
	v_mfma_scale_f32_16x16x128_f8f6f4 v[38:41], v[18:25], v[234:241], v[38:41], v191, v191 op_sel_hi:[0,0,0]
	v_mfma_scale_f32_16x16x128_f8f6f4 v[34:37], v[26:33], v[234:241], v[34:37], v191, v191 op_sel_hi:[0,0,0]
	s_setprio 0
	s_barrier
	s_add_i32 s92, s92, 2
	s_add_u32 s26, s26, 0x100
	s_addc_u32 s27, s27, 0
	s_add_u32 s65, s65, 0x100
	s_addc_u32 s74, s74, 0
	s_cmp_gt_u32 s92, 5
	s_cbranch_scc0 .LBB0_49
	s_and_b64 vcc, exec, s[42:43]
	s_cbranch_vccz .LBB0_52
	s_barrier

.LBB0_248:
	s_ashr_i32 s63, s62, 31
	s_lshl_b64 s[36:37], s[62:63], 21
	s_add_u32 s4, s82, s36
	s_addc_u32 s6, s83, s37
	s_ashr_i32 s61, s60, 31
	s_lshl_b64 s[36:37], s[60:61], 18
	s_add_u32 s64, s4, s36
	s_addc_u32 s65, s6, s37
	s_and_b64 s[36:37], s[70:71], exec
	s_cselect_b32 s6, s65, s27
	s_cselect_b32 s31, s64, s26
	v_mov_b32_e32 v173, v1
	v_mov_b32_e32 v175, v1
	s_add_u32 s61, s26, 0x100
	v_lshl_add_u64 v[176:177], s[54:55], 0, v[174:175]
	v_lshl_add_u64 v[178:179], s[54:55], 0, v[172:173]
	s_addc_u32 s63, s27, 0
	s_mov_b32 s67, -2
	s_mov_b64 s[26:27], 0
	s_add_u32 s4, s46, s26
	s_addc_u32 s36, s47, s27
	s_add_u32 s69, s4, 0x2e000100
	s_addc_u32 s70, s36, 0
	s_add_u32 s74, s61, s26
	s_addc_u32 s86, s63, s27
	s_add_i32 s4, 0, 0x10000
	s_cmpk_eq_i32 s26, 0x300
	s_cselect_b64 vcc, -1, 0
	s_and_b64 s[36:37], vcc, exec
	s_cselect_b32 s71, s41, s70
	s_cselect_b32 s70, s40, s69
	v_add_u32_e32 v0, s4, v200
	s_cselect_b32 s37, s6, s86
	s_cselect_b32 s36, s31, s74
	s_add_i32 s69, 0, 0x14000
	ds_read_b128 v[18:21], v0
	ds_read_b128 v[22:25], v0 offset:1024
	ds_read_b128 v[26:29], v0 offset:2048
	ds_read_b128 v[30:33], v0 offset:3072
	v_add_u32_e32 v0, s69, v200
	ds_read_b128 v[2:5], v0
	ds_read_b128 v[6:9], v0 offset:1024
	ds_read_b128 v[10:13], v0 offset:2048
	ds_read_b128 v[14:17], v0 offset:3072
	v_lshl_add_u64 v[222:223], v[178:179], 0, s[26:27]
	s_add_i32 m0, s93, 0xc000
	ds_read_b128 v[180:183], v201
	ds_read_b128 v[184:187], v201 offset:1024
	ds_read_b128 v[206:209], v201 offset:2048
	ds_read_b128 v[210:213], v201 offset:3072
	ds_read_b128 v[214:217], v201 offset:4096
	ds_read_b128 v[218:221], v201 offset:5120
	ds_read_b128 v[234:237], v201 offset:6144
	ds_read_b128 v[238:241], v201 offset:7168
	global_load_lds_dwordx4 v[222:223], off
	v_lshl_add_u64 v[222:223], v[176:177], 0, s[26:27]
	s_add_i32 m0, s93, 0xe000
	s_nop 0
	global_load_lds_dwordx4 v[222:223], off
	s_waitcnt vmcnt(8)
	s_waitcnt lgkmcnt(0)
	s_barrier
	s_setprio 1
	s_waitcnt lgkmcnt(0)
	v_mfma_scale_f32_16x16x128_f8f6f4 v[158:161], v[18:25], v[180:187], 0, v191, v191 op_sel_hi:[0,0,0]
	v_mfma_scale_f32_16x16x128_f8f6f4 v[154:157], v[26:33], v[180:187], 0, v191, v191 op_sel_hi:[0,0,0]
	v_mfma_scale_f32_16x16x128_f8f6f4 v[142:145], v[18:25], v[206:213], 0, v191, v191 op_sel_hi:[0,0,0]
	v_mfma_scale_f32_16x16x128_f8f6f4 v[138:141], v[26:33], v[206:213], 0, v191, v191 op_sel_hi:[0,0,0]
	v_mfma_scale_f32_16x16x128_f8f6f4 v[126:129], v[18:25], v[214:221], 0, v191, v191 op_sel_hi:[0,0,0]
	v_mfma_scale_f32_16x16x128_f8f6f4 v[122:125], v[26:33], v[214:221], 0, v191, v191 op_sel_hi:[0,0,0]
	v_mfma_scale_f32_16x16x128_f8f6f4 v[110:113], v[18:25], v[234:241], 0, v191, v191 op_sel_hi:[0,0,0]
	v_mfma_scale_f32_16x16x128_f8f6f4 v[106:109], v[26:33], v[234:241], 0, v191, v191 op_sel_hi:[0,0,0]
	v_mfma_scale_f32_16x16x128_f8f6f4 v[150:153], v[2:9], v[180:187], 0, v191, v191 op_sel_hi:[0,0,0]
	v_mfma_scale_f32_16x16x128_f8f6f4 v[146:149], v[10:17], v[180:187], 0, v191, v191 op_sel_hi:[0,0,0]
	v_mfma_scale_f32_16x16x128_f8f6f4 v[134:137], v[2:9], v[206:213], 0, v191, v191 op_sel_hi:[0,0,0]
	v_mfma_scale_f32_16x16x128_f8f6f4 v[130:133], v[10:17], v[206:213], 0, v191, v191 op_sel_hi:[0,0,0]
	v_mfma_scale_f32_16x16x128_f8f6f4 v[118:121], v[2:9], v[214:221], 0, v191, v191 op_sel_hi:[0,0,0]
	v_mfma_scale_f32_16x16x128_f8f6f4 v[114:117], v[10:17], v[214:221], 0, v191, v191 op_sel_hi:[0,0,0]
	v_mfma_scale_f32_16x16x128_f8f6f4 v[102:105], v[2:9], v[234:241], 0, v191, v191 op_sel_hi:[0,0,0]
	v_mfma_scale_f32_16x16x128_f8f6f4 v[98:101], v[10:17], v[234:241], 0, v191, v191 op_sel_hi:[0,0,0]
	s_setprio 0
	s_barrier
	s_add_i32 s4, s4, s92
	v_lshl_add_u64 v[180:181], s[36:37], 0, v[162:163]
	s_mov_b32 m0, s4
	ds_read_b128 v[206:209], v201 offset:16384
	ds_read_b128 v[210:213], v201 offset:17408
	ds_read_b128 v[214:217], v201 offset:18432
	ds_read_b128 v[218:221], v201 offset:19456
	ds_read_b128 v[234:237], v201 offset:20480
	ds_read_b128 v[238:241], v201 offset:21504
	ds_read_b128 v[242:245], v201 offset:22528
	ds_read_b128 v[246:249], v201 offset:23552
	global_load_lds_dwordx4 v[180:181], off
	s_add_i32 m0, s4, 0x2000
	s_add_u32 s86, s36, 0x20000
	v_lshl_add_u64 v[182:183], s[36:37], 0, v[164:165]
	s_addc_u32 s87, s37, 0
	s_add_i32 s4, s69, s92
	global_load_lds_dwordx4 v[182:183], off
	v_lshl_add_u64 v[184:185], s[86:87], 0, v[162:163]
	s_mov_b32 m0, s4
	v_cndmask_b32_e32 v0, v168, v202, vcc
	global_load_lds_dwordx4 v[184:185], off
	v_lshl_add_u64 v[184:185], s[86:87], 0, v[164:165]
	s_add_i32 m0, s4, 0x2000
	v_lshl_add_u64 v[186:187], s[70:71], 0, v[0:1]
	global_load_lds_dwordx4 v[184:185], off
	s_mov_b32 m0, s93
	v_cndmask_b32_e32 v184, v170, v203, vcc
	global_load_lds_dwordx4 v0, s[70:71]
	s_mov_b32 m0, s79
	v_mov_b32_e32 v185, v1
	global_load_lds_dwordx4 v184, s[70:71]
	s_waitcnt vmcnt(8)
	s_waitcnt lgkmcnt(0)
	v_lshl_add_u64 v[184:185], s[70:71], 0, v[184:185]
	s_barrier
	s_setprio 1
	s_waitcnt lgkmcnt(0)
	v_mfma_scale_f32_16x16x128_f8f6f4 v[94:97], v[18:25], v[206:213], 0, v191, v191 op_sel_hi:[0,0,0]
	v_mfma_scale_f32_16x16x128_f8f6f4 v[90:93], v[26:33], v[206:213], 0, v191, v191 op_sel_hi:[0,0,0]
	v_mfma_scale_f32_16x16x128_f8f6f4 v[70:73], v[18:25], v[214:221], 0, v191, v191 op_sel_hi:[0,0,0]
	v_mfma_scale_f32_16x16x128_f8f6f4 v[66:69], v[26:33], v[214:221], 0, v191, v191 op_sel_hi:[0,0,0]
	v_mfma_scale_f32_16x16x128_f8f6f4 v[54:57], v[18:25], v[234:241], 0, v191, v191 op_sel_hi:[0,0,0]
	v_mfma_scale_f32_16x16x128_f8f6f4 v[50:53], v[26:33], v[234:241], 0, v191, v191 op_sel_hi:[0,0,0]
	v_mfma_scale_f32_16x16x128_f8f6f4 v[38:41], v[18:25], v[242:249], 0, v191, v191 op_sel_hi:[0,0,0]
	v_mfma_scale_f32_16x16x128_f8f6f4 v[34:37], v[26:33], v[242:249], 0, v191, v191 op_sel_hi:[0,0,0]
	v_mfma_scale_f32_16x16x128_f8f6f4 v[86:89], v[2:9], v[206:213], 0, v191, v191 op_sel_hi:[0,0,0]
	v_mfma_scale_f32_16x16x128_f8f6f4 v[82:85], v[10:17], v[206:213], 0, v191, v191 op_sel_hi:[0,0,0]
	v_mfma_scale_f32_16x16x128_f8f6f4 v[78:81], v[2:9], v[214:221], 0, v191, v191 op_sel_hi:[0,0,0]
	v_mfma_scale_f32_16x16x128_f8f6f4 v[74:77], v[10:17], v[214:221], 0, v191, v191 op_sel_hi:[0,0,0]
	v_mfma_scale_f32_16x16x128_f8f6f4 v[62:65], v[2:9], v[234:241], 0, v191, v191 op_sel_hi:[0,0,0]
	v_mfma_scale_f32_16x16x128_f8f6f4 v[58:61], v[10:17], v[234:241], 0, v191, v191 op_sel_hi:[0,0,0]
	v_mfma_scale_f32_16x16x128_f8f6f4 v[46:49], v[2:9], v[242:249], 0, v191, v191 op_sel_hi:[0,0,0]
	v_mfma_scale_f32_16x16x128_f8f6f4 v[42:45], v[10:17], v[242:249], 0, v191, v191 op_sel_hi:[0,0,0]
	s_setprio 0
	s_barrier
	s_add_i32 s4, 0, 0x18000
	v_add_u32_e32 v0, s4, v200
	s_add_i32 s69, 0, 0x1c000
	ds_read_b128 v[2:5], v0
	ds_read_b128 v[6:9], v0 offset:1024
	ds_read_b128 v[10:13], v0 offset:2048
	ds_read_b128 v[14:17], v0 offset:3072
	v_add_u32_e32 v0, s69, v200
	ds_read_b128 v[18:21], v0
	ds_read_b128 v[22:25], v0 offset:1024
	ds_read_b128 v[26:29], v0 offset:2048
	ds_read_b128 v[30:33], v0 offset:3072
	s_mov_b32 m0, s84
	v_cndmask_b32_e32 v0, v172, v204, vcc
	ds_read_b128 v[206:209], v201 offset:32768
	ds_read_b128 v[210:213], v201 offset:33792
	ds_read_b128 v[214:217], v201 offset:34816
	ds_read_b128 v[218:221], v201 offset:35840
	ds_read_b128 v[234:237], v201 offset:36864
	ds_read_b128 v[238:241], v201 offset:37888
	ds_read_b128 v[242:245], v201 offset:38912
	ds_read_b128 v[246:249], v201 offset:39936
	v_cndmask_b32_e32 v173, v174, v205, vcc
	global_load_lds_dwordx4 v0, s[70:71]
	s_mov_b32 m0, s85
	s_nop 0
	global_load_lds_dwordx4 v173, s[70:71]
	s_waitcnt vmcnt(8)
	s_waitcnt lgkmcnt(0)
	s_barrier
	s_setprio 1
	s_waitcnt lgkmcnt(0)
	v_mfma_scale_f32_16x16x128_f8f6f4 v[158:161], v[2:9], v[206:213], v[158:161], v191, v191 op_sel_hi:[0,0,0]
	v_mfma_scale_f32_16x16x128_f8f6f4 v[154:157], v[10:17], v[206:213], v[154:157], v191, v191 op_sel_hi:[0,0,0]
	v_mfma_scale_f32_16x16x128_f8f6f4 v[142:145], v[2:9], v[214:221], v[142:145], v191, v191 op_sel_hi:[0,0,0]
	v_mfma_scale_f32_16x16x128_f8f6f4 v[138:141], v[10:17], v[214:221], v[138:141], v191, v191 op_sel_hi:[0,0,0]
	v_mfma_scale_f32_16x16x128_f8f6f4 v[126:129], v[2:9], v[234:241], v[126:129], v191, v191 op_sel_hi:[0,0,0]
	v_mfma_scale_f32_16x16x128_f8f6f4 v[122:125], v[10:17], v[234:241], v[122:125], v191, v191 op_sel_hi:[0,0,0]
	v_mfma_scale_f32_16x16x128_f8f6f4 v[110:113], v[2:9], v[242:249], v[110:113], v191, v191 op_sel_hi:[0,0,0]
	v_mfma_scale_f32_16x16x128_f8f6f4 v[106:109], v[10:17], v[242:249], v[106:109], v191, v191 op_sel_hi:[0,0,0]
	v_mfma_scale_f32_16x16x128_f8f6f4 v[150:153], v[18:25], v[206:213], v[150:153], v191, v191 op_sel_hi:[0,0,0]
	v_mfma_scale_f32_16x16x128_f8f6f4 v[146:149], v[26:33], v[206:213], v[146:149], v191, v191 op_sel_hi:[0,0,0]
	v_mfma_scale_f32_16x16x128_f8f6f4 v[134:137], v[18:25], v[214:221], v[134:137], v191, v191 op_sel_hi:[0,0,0]
	v_mfma_scale_f32_16x16x128_f8f6f4 v[130:133], v[26:33], v[214:221], v[130:133], v191, v191 op_sel_hi:[0,0,0]
	v_mfma_scale_f32_16x16x128_f8f6f4 v[118:121], v[18:25], v[234:241], v[118:121], v191, v191 op_sel_hi:[0,0,0]
	v_mfma_scale_f32_16x16x128_f8f6f4 v[114:117], v[26:33], v[234:241], v[114:117], v191, v191 op_sel_hi:[0,0,0]
	v_mfma_scale_f32_16x16x128_f8f6f4 v[102:105], v[18:25], v[242:249], v[102:105], v191, v191 op_sel_hi:[0,0,0]
	v_mfma_scale_f32_16x16x128_f8f6f4 v[98:101], v[26:33], v[242:249], v[98:101], v191, v191 op_sel_hi:[0,0,0]
	s_setprio 0
	s_barrier
	s_add_i32 s4, s4, s92
	v_lshl_add_u64 v[180:181], v[180:181], 0, s[22:23]
	s_mov_b32 m0, s4
	ds_read_b128 v[206:209], v201 offset:49152
	ds_read_b128 v[210:213], v201 offset:50176
	ds_read_b128 v[214:217], v201 offset:51200
	ds_read_b128 v[218:221], v201 offset:52224
	ds_read_b128 v[234:237], v201 offset:53248
	ds_read_b128 v[238:241], v201 offset:54272
	ds_read_b128 v[242:245], v201 offset:55296
	ds_read_b128 v[246:249], v201 offset:56320
	global_load_lds_dwordx4 v[180:181], off
	s_add_i32 m0, s4, 0x2000
	s_add_u32 s36, s36, 0x20080
	v_lshl_add_u64 v[180:181], v[182:183], 0, s[22:23]
	s_addc_u32 s37, s37, 0
	s_add_i32 s4, s69, s92
	global_load_lds_dwordx4 v[180:181], off
	v_lshl_add_u64 v[180:181], s[36:37], 0, v[162:163]
	s_mov_b32 m0, s4
	s_nop 0
	global_load_lds_dwordx4 v[180:181], off
	v_lshl_add_u64 v[180:181], s[36:37], 0, v[164:165]
	s_add_i32 m0, s4, 0x2000
	s_nop 0
	global_load_lds_dwordx4 v[180:181], off
	v_lshl_add_u64 v[180:181], v[186:187], 0, s[22:23]
	s_mov_b32 m0, s15
	s_nop 0
	global_load_lds_dwordx4 v[180:181], off
	v_lshl_add_u64 v[180:181], v[184:185], 0, s[22:23]
	s_mov_b32 m0, s16
	s_nop 0
	global_load_lds_dwordx4 v[180:181], off
	s_waitcnt vmcnt(8)
	s_waitcnt lgkmcnt(0)
	s_barrier
	s_setprio 1
	s_waitcnt lgkmcnt(0)
	v_mfma_scale_f32_16x16x128_f8f6f4 v[94:97], v[2:9], v[206:213], v[94:97], v191, v191 op_sel_hi:[0,0,0]
	v_mfma_scale_f32_16x16x128_f8f6f4 v[90:93], v[10:17], v[206:213], v[90:93], v191, v191 op_sel_hi:[0,0,0]
	v_mfma_scale_f32_16x16x128_f8f6f4 v[70:73], v[2:9], v[214:221], v[70:73], v191, v191 op_sel_hi:[0,0,0]
	v_mfma_scale_f32_16x16x128_f8f6f4 v[66:69], v[10:17], v[214:221], v[66:69], v191, v191 op_sel_hi:[0,0,0]
	v_mfma_scale_f32_16x16x128_f8f6f4 v[54:57], v[2:9], v[234:241], v[54:57], v191, v191 op_sel_hi:[0,0,0]
	v_mfma_scale_f32_16x16x128_f8f6f4 v[50:53], v[10:17], v[234:241], v[50:53], v191, v191 op_sel_hi:[0,0,0]
	v_mfma_scale_f32_16x16x128_f8f6f4 v[38:41], v[2:9], v[242:249], v[38:41], v191, v191 op_sel_hi:[0,0,0]
	v_mfma_scale_f32_16x16x128_f8f6f4 v[34:37], v[10:17], v[242:249], v[34:37], v191, v191 op_sel_hi:[0,0,0]
	v_mfma_scale_f32_16x16x128_f8f6f4 v[86:89], v[18:25], v[206:213], v[86:89], v191, v191 op_sel_hi:[0,0,0]
	v_mfma_scale_f32_16x16x128_f8f6f4 v[82:85], v[26:33], v[206:213], v[82:85], v191, v191 op_sel_hi:[0,0,0]
	v_mfma_scale_f32_16x16x128_f8f6f4 v[78:81], v[18:25], v[214:221], v[78:81], v191, v191 op_sel_hi:[0,0,0]
	v_mfma_scale_f32_16x16x128_f8f6f4 v[74:77], v[26:33], v[214:221], v[74:77], v191, v191 op_sel_hi:[0,0,0]
	v_mfma_scale_f32_16x16x128_f8f6f4 v[62:65], v[18:25], v[234:241], v[62:65], v191, v191 op_sel_hi:[0,0,0]
	v_mfma_scale_f32_16x16x128_f8f6f4 v[58:61], v[26:33], v[234:241], v[58:61], v191, v191 op_sel_hi:[0,0,0]
	v_mfma_scale_f32_16x16x128_f8f6f4 v[46:49], v[18:25], v[242:249], v[46:49], v191, v191 op_sel_hi:[0,0,0]
	v_mfma_scale_f32_16x16x128_f8f6f4 v[42:45], v[26:33], v[242:249], v[42:45], v191, v191 op_sel_hi:[0,0,0]
	s_setprio 0
	s_barrier
	s_add_i32 s67, s67, 2
	s_add_u32 s26, s26, 0x100
	s_addc_u32 s27, s27, 0
.LBB0_249:
	s_add_u32 s4, s46, s26
	s_addc_u32 s36, s47, s27
	s_add_u32 s69, s4, 0x2e000100
	s_addc_u32 s70, s36, 0
	s_add_u32 s74, s61, s26
	s_addc_u32 s86, s63, s27
	s_add_i32 s4, 0, 0x10000
	s_cmpk_eq_i32 s26, 0x300
	s_cselect_b64 vcc, -1, 0
	s_and_b64 s[36:37], vcc, exec
	s_cselect_b32 s71, s41, s70
	s_cselect_b32 s70, s40, s69
	v_add_u32_e32 v0, s4, v200
	s_cselect_b32 s37, s6, s86
	s_cselect_b32 s36, s31, s74
	s_add_i32 s69, 0, 0x14000
	ds_read_b128 v[18:21], v0
	ds_read_b128 v[22:25], v0 offset:1024
	ds_read_b128 v[26:29], v0 offset:2048
	ds_read_b128 v[30:33], v0 offset:3072
	v_add_u32_e32 v0, s69, v200
	ds_read_b128 v[2:5], v0
	ds_read_b128 v[6:9], v0 offset:1024
	ds_read_b128 v[10:13], v0 offset:2048
	ds_read_b128 v[14:17], v0 offset:3072
	v_lshl_add_u64 v[222:223], v[178:179], 0, s[26:27]
	s_add_i32 m0, s93, 0xc000
	ds_read_b128 v[180:183], v201
	ds_read_b128 v[184:187], v201 offset:1024
	ds_read_b128 v[206:209], v201 offset:2048
	ds_read_b128 v[210:213], v201 offset:3072
	ds_read_b128 v[214:217], v201 offset:4096
	ds_read_b128 v[218:221], v201 offset:5120
	ds_read_b128 v[234:237], v201 offset:6144
	ds_read_b128 v[238:241], v201 offset:7168
	global_load_lds_dwordx4 v[222:223], off
	v_lshl_add_u64 v[222:223], v[176:177], 0, s[26:27]
	s_add_i32 m0, s93, 0xe000
	s_nop 0
	global_load_lds_dwordx4 v[222:223], off
	s_waitcnt vmcnt(8)
	s_waitcnt lgkmcnt(0)
	s_barrier
	s_setprio 1
	s_waitcnt lgkmcnt(0)
	v_mfma_scale_f32_16x16x128_f8f6f4 v[158:161], v[18:25], v[180:187], v[158:161], v191, v191 op_sel_hi:[0,0,0]
	v_mfma_scale_f32_16x16x128_f8f6f4 v[154:157], v[26:33], v[180:187], v[154:157], v191, v191 op_sel_hi:[0,0,0]
	v_mfma_scale_f32_16x16x128_f8f6f4 v[142:145], v[18:25], v[206:213], v[142:145], v191, v191 op_sel_hi:[0,0,0]
	v_mfma_scale_f32_16x16x128_f8f6f4 v[138:141], v[26:33], v[206:213], v[138:141], v191, v191 op_sel_hi:[0,0,0]
	v_mfma_scale_f32_16x16x128_f8f6f4 v[126:129], v[18:25], v[214:221], v[126:129], v191, v191 op_sel_hi:[0,0,0]
	v_mfma_scale_f32_16x16x128_f8f6f4 v[122:125], v[26:33], v[214:221], v[122:125], v191, v191 op_sel_hi:[0,0,0]
	v_mfma_scale_f32_16x16x128_f8f6f4 v[110:113], v[18:25], v[234:241], v[110:113], v191, v191 op_sel_hi:[0,0,0]
	v_mfma_scale_f32_16x16x128_f8f6f4 v[106:109], v[26:33], v[234:241], v[106:109], v191, v191 op_sel_hi:[0,0,0]
	v_mfma_scale_f32_16x16x128_f8f6f4 v[150:153], v[2:9], v[180:187], v[150:153], v191, v191 op_sel_hi:[0,0,0]
	v_mfma_scale_f32_16x16x128_f8f6f4 v[146:149], v[10:17], v[180:187], v[146:149], v191, v191 op_sel_hi:[0,0,0]
	v_mfma_scale_f32_16x16x128_f8f6f4 v[134:137], v[2:9], v[206:213], v[134:137], v191, v191 op_sel_hi:[0,0,0]
	v_mfma_scale_f32_16x16x128_f8f6f4 v[130:133], v[10:17], v[206:213], v[130:133], v191, v191 op_sel_hi:[0,0,0]
	v_mfma_scale_f32_16x16x128_f8f6f4 v[118:121], v[2:9], v[214:221], v[118:121], v191, v191 op_sel_hi:[0,0,0]
	v_mfma_scale_f32_16x16x128_f8f6f4 v[114:117], v[10:17], v[214:221], v[114:117], v191, v191 op_sel_hi:[0,0,0]
	v_mfma_scale_f32_16x16x128_f8f6f4 v[102:105], v[2:9], v[234:241], v[102:105], v191, v191 op_sel_hi:[0,0,0]
	v_mfma_scale_f32_16x16x128_f8f6f4 v[98:101], v[10:17], v[234:241], v[98:101], v191, v191 op_sel_hi:[0,0,0]
	s_setprio 0
	s_barrier
	s_add_i32 s4, s4, s92
	v_lshl_add_u64 v[180:181], s[36:37], 0, v[162:163]
	s_mov_b32 m0, s4
	ds_read_b128 v[206:209], v201 offset:16384
	ds_read_b128 v[210:213], v201 offset:17408
	ds_read_b128 v[214:217], v201 offset:18432
	ds_read_b128 v[218:221], v201 offset:19456
	ds_read_b128 v[234:237], v201 offset:20480
	ds_read_b128 v[238:241], v201 offset:21504
	ds_read_b128 v[242:245], v201 offset:22528
	ds_read_b128 v[246:249], v201 offset:23552
	global_load_lds_dwordx4 v[180:181], off
	s_add_i32 m0, s4, 0x2000
	s_add_u32 s86, s36, 0x20000
	v_lshl_add_u64 v[182:183], s[36:37], 0, v[164:165]
	s_addc_u32 s87, s37, 0
	s_add_i32 s4, s69, s92
	global_load_lds_dwordx4 v[182:183], off
	v_lshl_add_u64 v[184:185], s[86:87], 0, v[162:163]
	s_mov_b32 m0, s4
	v_cndmask_b32_e32 v0, v168, v202, vcc
	global_load_lds_dwordx4 v[184:185], off
	v_lshl_add_u64 v[184:185], s[86:87], 0, v[164:165]
	s_add_i32 m0, s4, 0x2000
	v_lshl_add_u64 v[186:187], s[70:71], 0, v[0:1]
	global_load_lds_dwordx4 v[184:185], off
	s_mov_b32 m0, s93
	v_cndmask_b32_e32 v184, v170, v203, vcc
	global_load_lds_dwordx4 v0, s[70:71]
	s_mov_b32 m0, s79
	v_mov_b32_e32 v185, v1
	global_load_lds_dwordx4 v184, s[70:71]
	s_waitcnt vmcnt(8)
	s_waitcnt lgkmcnt(0)
	v_lshl_add_u64 v[184:185], s[70:71], 0, v[184:185]
	s_barrier
	s_setprio 1
	s_waitcnt lgkmcnt(0)
	v_mfma_scale_f32_16x16x128_f8f6f4 v[94:97], v[18:25], v[206:213], v[94:97], v191, v191 op_sel_hi:[0,0,0]
	v_mfma_scale_f32_16x16x128_f8f6f4 v[90:93], v[26:33], v[206:213], v[90:93], v191, v191 op_sel_hi:[0,0,0]
	v_mfma_scale_f32_16x16x128_f8f6f4 v[70:73], v[18:25], v[214:221], v[70:73], v191, v191 op_sel_hi:[0,0,0]
	v_mfma_scale_f32_16x16x128_f8f6f4 v[66:69], v[26:33], v[214:221], v[66:69], v191, v191 op_sel_hi:[0,0,0]
	v_mfma_scale_f32_16x16x128_f8f6f4 v[54:57], v[18:25], v[234:241], v[54:57], v191, v191 op_sel_hi:[0,0,0]
	v_mfma_scale_f32_16x16x128_f8f6f4 v[50:53], v[26:33], v[234:241], v[50:53], v191, v191 op_sel_hi:[0,0,0]
	v_mfma_scale_f32_16x16x128_f8f6f4 v[38:41], v[18:25], v[242:249], v[38:41], v191, v191 op_sel_hi:[0,0,0]
	v_mfma_scale_f32_16x16x128_f8f6f4 v[34:37], v[26:33], v[242:249], v[34:37], v191, v191 op_sel_hi:[0,0,0]
	v_mfma_scale_f32_16x16x128_f8f6f4 v[86:89], v[2:9], v[206:213], v[86:89], v191, v191 op_sel_hi:[0,0,0]
	v_mfma_scale_f32_16x16x128_f8f6f4 v[82:85], v[10:17], v[206:213], v[82:85], v191, v191 op_sel_hi:[0,0,0]
	v_mfma_scale_f32_16x16x128_f8f6f4 v[78:81], v[2:9], v[214:221], v[78:81], v191, v191 op_sel_hi:[0,0,0]
	v_mfma_scale_f32_16x16x128_f8f6f4 v[74:77], v[10:17], v[214:221], v[74:77], v191, v191 op_sel_hi:[0,0,0]
	v_mfma_scale_f32_16x16x128_f8f6f4 v[62:65], v[2:9], v[234:241], v[62:65], v191, v191 op_sel_hi:[0,0,0]
	v_mfma_scale_f32_16x16x128_f8f6f4 v[58:61], v[10:17], v[234:241], v[58:61], v191, v191 op_sel_hi:[0,0,0]
	v_mfma_scale_f32_16x16x128_f8f6f4 v[46:49], v[2:9], v[242:249], v[46:49], v191, v191 op_sel_hi:[0,0,0]
	v_mfma_scale_f32_16x16x128_f8f6f4 v[42:45], v[10:17], v[242:249], v[42:45], v191, v191 op_sel_hi:[0,0,0]
	s_setprio 0
	s_barrier
	s_add_i32 s4, 0, 0x18000
	v_add_u32_e32 v0, s4, v200
	s_add_i32 s69, 0, 0x1c000
	ds_read_b128 v[2:5], v0
	ds_read_b128 v[6:9], v0 offset:1024
	ds_read_b128 v[10:13], v0 offset:2048
	ds_read_b128 v[14:17], v0 offset:3072
	v_add_u32_e32 v0, s69, v200
	ds_read_b128 v[18:21], v0
	ds_read_b128 v[22:25], v0 offset:1024
	ds_read_b128 v[26:29], v0 offset:2048
	ds_read_b128 v[30:33], v0 offset:3072
	s_mov_b32 m0, s84
	v_cndmask_b32_e32 v0, v172, v204, vcc
	ds_read_b128 v[206:209], v201 offset:32768
	ds_read_b128 v[210:213], v201 offset:33792
	ds_read_b128 v[214:217], v201 offset:34816
	ds_read_b128 v[218:221], v201 offset:35840
	ds_read_b128 v[234:237], v201 offset:36864
	ds_read_b128 v[238:241], v201 offset:37888
	ds_read_b128 v[242:245], v201 offset:38912
	ds_read_b128 v[246:249], v201 offset:39936
	v_cndmask_b32_e32 v173, v174, v205, vcc
	global_load_lds_dwordx4 v0, s[70:71]
	s_mov_b32 m0, s85
	s_nop 0
	global_load_lds_dwordx4 v173, s[70:71]
	s_waitcnt vmcnt(8)
	s_waitcnt lgkmcnt(0)
	s_barrier
	s_setprio 1
	s_waitcnt lgkmcnt(0)
	v_mfma_scale_f32_16x16x128_f8f6f4 v[158:161], v[2:9], v[206:213], v[158:161], v191, v191 op_sel_hi:[0,0,0]
	v_mfma_scale_f32_16x16x128_f8f6f4 v[154:157], v[10:17], v[206:213], v[154:157], v191, v191 op_sel_hi:[0,0,0]
	v_mfma_scale_f32_16x16x128_f8f6f4 v[142:145], v[2:9], v[214:221], v[142:145], v191, v191 op_sel_hi:[0,0,0]
	v_mfma_scale_f32_16x16x128_f8f6f4 v[138:141], v[10:17], v[214:221], v[138:141], v191, v191 op_sel_hi:[0,0,0]
	v_mfma_scale_f32_16x16x128_f8f6f4 v[126:129], v[2:9], v[234:241], v[126:129], v191, v191 op_sel_hi:[0,0,0]
	v_mfma_scale_f32_16x16x128_f8f6f4 v[122:125], v[10:17], v[234:241], v[122:125], v191, v191 op_sel_hi:[0,0,0]
	v_mfma_scale_f32_16x16x128_f8f6f4 v[110:113], v[2:9], v[242:249], v[110:113], v191, v191 op_sel_hi:[0,0,0]
	v_mfma_scale_f32_16x16x128_f8f6f4 v[106:109], v[10:17], v[242:249], v[106:109], v191, v191 op_sel_hi:[0,0,0]
	v_mfma_scale_f32_16x16x128_f8f6f4 v[150:153], v[18:25], v[206:213], v[150:153], v191, v191 op_sel_hi:[0,0,0]
	v_mfma_scale_f32_16x16x128_f8f6f4 v[146:149], v[26:33], v[206:213], v[146:149], v191, v191 op_sel_hi:[0,0,0]
	v_mfma_scale_f32_16x16x128_f8f6f4 v[134:137], v[18:25], v[214:221], v[134:137], v191, v191 op_sel_hi:[0,0,0]
	v_mfma_scale_f32_16x16x128_f8f6f4 v[130:133], v[26:33], v[214:221], v[130:133], v191, v191 op_sel_hi:[0,0,0]
	v_mfma_scale_f32_16x16x128_f8f6f4 v[118:121], v[18:25], v[234:241], v[118:121], v191, v191 op_sel_hi:[0,0,0]
	v_mfma_scale_f32_16x16x128_f8f6f4 v[114:117], v[26:33], v[234:241], v[114:117], v191, v191 op_sel_hi:[0,0,0]
	v_mfma_scale_f32_16x16x128_f8f6f4 v[102:105], v[18:25], v[242:249], v[102:105], v191, v191 op_sel_hi:[0,0,0]
	v_mfma_scale_f32_16x16x128_f8f6f4 v[98:101], v[26:33], v[242:249], v[98:101], v191, v191 op_sel_hi:[0,0,0]
	s_setprio 0
	s_barrier
	s_add_i32 s4, s4, s92
	v_lshl_add_u64 v[180:181], v[180:181], 0, s[22:23]
	s_mov_b32 m0, s4
	ds_read_b128 v[206:209], v201 offset:49152
	ds_read_b128 v[210:213], v201 offset:50176
	ds_read_b128 v[214:217], v201 offset:51200
	ds_read_b128 v[218:221], v201 offset:52224
	ds_read_b128 v[234:237], v201 offset:53248
	ds_read_b128 v[238:241], v201 offset:54272
	ds_read_b128 v[242:245], v201 offset:55296
	ds_read_b128 v[246:249], v201 offset:56320
	global_load_lds_dwordx4 v[180:181], off
	s_add_i32 m0, s4, 0x2000
	s_add_u32 s36, s36, 0x20080
	v_lshl_add_u64 v[180:181], v[182:183], 0, s[22:23]
	s_addc_u32 s37, s37, 0
	s_add_i32 s4, s69, s92
	global_load_lds_dwordx4 v[180:181], off
	v_lshl_add_u64 v[180:181], s[36:37], 0, v[162:163]
	s_mov_b32 m0, s4
	s_nop 0
	global_load_lds_dwordx4 v[180:181], off
	v_lshl_add_u64 v[180:181], s[36:37], 0, v[164:165]
	s_add_i32 m0, s4, 0x2000
	s_nop 0
	global_load_lds_dwordx4 v[180:181], off
	v_lshl_add_u64 v[180:181], v[186:187], 0, s[22:23]
	s_mov_b32 m0, s15
	s_nop 0
	global_load_lds_dwordx4 v[180:181], off
	v_lshl_add_u64 v[180:181], v[184:185], 0, s[22:23]
	s_mov_b32 m0, s16
	s_nop 0
	global_load_lds_dwordx4 v[180:181], off
	s_waitcnt vmcnt(8)
	s_waitcnt lgkmcnt(0)
	s_barrier
	s_setprio 1
	s_waitcnt lgkmcnt(0)
	v_mfma_scale_f32_16x16x128_f8f6f4 v[94:97], v[2:9], v[206:213], v[94:97], v191, v191 op_sel_hi:[0,0,0]
	v_mfma_scale_f32_16x16x128_f8f6f4 v[90:93], v[10:17], v[206:213], v[90:93], v191, v191 op_sel_hi:[0,0,0]
	v_mfma_scale_f32_16x16x128_f8f6f4 v[70:73], v[2:9], v[214:221], v[70:73], v191, v191 op_sel_hi:[0,0,0]
	v_mfma_scale_f32_16x16x128_f8f6f4 v[66:69], v[10:17], v[214:221], v[66:69], v191, v191 op_sel_hi:[0,0,0]
	v_mfma_scale_f32_16x16x128_f8f6f4 v[54:57], v[2:9], v[234:241], v[54:57], v191, v191 op_sel_hi:[0,0,0]
	v_mfma_scale_f32_16x16x128_f8f6f4 v[50:53], v[10:17], v[234:241], v[50:53], v191, v191 op_sel_hi:[0,0,0]
	v_mfma_scale_f32_16x16x128_f8f6f4 v[38:41], v[2:9], v[242:249], v[38:41], v191, v191 op_sel_hi:[0,0,0]
	v_mfma_scale_f32_16x16x128_f8f6f4 v[34:37], v[10:17], v[242:249], v[34:37], v191, v191 op_sel_hi:[0,0,0]
	v_mfma_scale_f32_16x16x128_f8f6f4 v[86:89], v[18:25], v[206:213], v[86:89], v191, v191 op_sel_hi:[0,0,0]
	v_mfma_scale_f32_16x16x128_f8f6f4 v[82:85], v[26:33], v[206:213], v[82:85], v191, v191 op_sel_hi:[0,0,0]
	v_mfma_scale_f32_16x16x128_f8f6f4 v[78:81], v[18:25], v[214:221], v[78:81], v191, v191 op_sel_hi:[0,0,0]
	v_mfma_scale_f32_16x16x128_f8f6f4 v[74:77], v[26:33], v[214:221], v[74:77], v191, v191 op_sel_hi:[0,0,0]
	v_mfma_scale_f32_16x16x128_f8f6f4 v[62:65], v[18:25], v[234:241], v[62:65], v191, v191 op_sel_hi:[0,0,0]
	v_mfma_scale_f32_16x16x128_f8f6f4 v[58:61], v[26:33], v[234:241], v[58:61], v191, v191 op_sel_hi:[0,0,0]
	v_mfma_scale_f32_16x16x128_f8f6f4 v[46:49], v[18:25], v[242:249], v[46:49], v191, v191 op_sel_hi:[0,0,0]
	v_mfma_scale_f32_16x16x128_f8f6f4 v[42:45], v[26:33], v[242:249], v[42:45], v191, v191 op_sel_hi:[0,0,0]
	s_setprio 0
	s_barrier
	s_add_i32 s67, s67, 2
	s_add_u32 s26, s26, 0x100
	s_addc_u32 s27, s27, 0
	s_cmp_gt_u32 s67, 5
	s_cbranch_scc0 .LBB0_249
	s_and_b64 vcc, exec, s[58:59]
	s_cbranch_vccz .LBB0_252
	s_barrier

.LBB0_508:
	s_add_u32 s4, s50, 0xfffc0080
	s_addc_u32 s52, s51, -1
	s_add_i32 s69, 0, 0x10000
	s_cmp_eq_u32 s68, 12
	s_cselect_b32 s55, s47, s52
	s_cselect_b32 s54, s64, s4
	s_cselect_b32 s53, s45, s67
	s_cselect_b32 s52, s65, s66
	s_add_i32 s4, 0, 0x14000
	v_add_u32_e32 v142, s69, v195
	v_add_u32_e32 v158, s4, v195
	ds_read_b128 v[130:133], v142
	ds_read_b128 v[134:137], v142 offset:1024
	ds_read_b128 v[138:141], v142 offset:2048
	ds_read_b128 v[142:145], v142 offset:3072
	ds_read_b128 v[146:149], v158
	ds_read_b128 v[150:153], v158 offset:1024
	ds_read_b128 v[154:157], v158 offset:2048
	ds_read_b128 v[158:161], v158 offset:3072
	v_lshl_add_u64 v[210:211], s[50:51], 0, v[202:203]
	s_add_i32 m0, s49, 0xc000
	ds_read_b128 v[162:165], v234
	ds_read_b128 v[166:169], v234 offset:1024
	ds_read_b128 v[170:173], v234 offset:2048
	ds_read_b128 v[174:177], v234 offset:3072
	ds_read_b128 v[178:181], v234 offset:4096
	ds_read_b128 v[182:185], v234 offset:5120
	ds_read_b128 v[186:189], v234 offset:6144
	ds_read_b128 v[206:209], v234 offset:7168
	global_load_lds_dwordx4 v[210:211], off
	v_lshl_add_u64 v[210:211], s[50:51], 0, v[204:205]
	s_add_i32 m0, s49, 0xe000
	s_nop 0
	global_load_lds_dwordx4 v[210:211], off
	s_waitcnt vmcnt(8)
	s_waitcnt lgkmcnt(0)
	s_barrier
	s_setprio 1
	s_waitcnt lgkmcnt(0)
	v_mfma_f32_16x16x32_bf16 v[126:129], v[130:133], v[162:165], v[126:129]
	v_mfma_f32_16x16x32_bf16 v[122:125], v[138:141], v[162:165], v[122:125]
	v_mfma_f32_16x16x32_bf16 v[110:113], v[130:133], v[170:173], v[110:113]
	v_mfma_f32_16x16x32_bf16 v[106:109], v[138:141], v[170:173], v[106:109]
	v_mfma_f32_16x16x32_bf16 v[98:101], v[130:133], v[178:181], v[98:101]
	v_mfma_f32_16x16x32_bf16 v[90:93], v[138:141], v[178:181], v[90:93]
	v_mfma_f32_16x16x32_bf16 v[82:85], v[130:133], v[186:189], v[82:85]
	v_mfma_f32_16x16x32_bf16 v[74:77], v[138:141], v[186:189], v[74:77]
	v_mfma_f32_16x16x32_bf16 v[126:129], v[134:137], v[166:169], v[126:129]
	v_mfma_f32_16x16x32_bf16 v[122:125], v[142:145], v[166:169], v[122:125]
	v_mfma_f32_16x16x32_bf16 v[110:113], v[134:137], v[174:177], v[110:113]
	v_mfma_f32_16x16x32_bf16 v[106:109], v[142:145], v[174:177], v[106:109]
	v_mfma_f32_16x16x32_bf16 v[98:101], v[134:137], v[182:185], v[98:101]
	v_mfma_f32_16x16x32_bf16 v[90:93], v[142:145], v[182:185], v[90:93]
	v_mfma_f32_16x16x32_bf16 v[82:85], v[134:137], v[206:209], v[82:85]
	v_mfma_f32_16x16x32_bf16 v[74:77], v[142:145], v[206:209], v[74:77]
	v_mfma_f32_16x16x32_bf16 v[118:121], v[146:149], v[162:165], v[118:121]
	v_mfma_f32_16x16x32_bf16 v[114:117], v[154:157], v[162:165], v[114:117]
	v_mfma_f32_16x16x32_bf16 v[102:105], v[146:149], v[170:173], v[102:105]
	v_mfma_f32_16x16x32_bf16 v[94:97], v[154:157], v[170:173], v[94:97]
	v_mfma_f32_16x16x32_bf16 v[86:89], v[146:149], v[178:181], v[86:89]
	v_mfma_f32_16x16x32_bf16 v[78:81], v[154:157], v[178:181], v[78:81]
	v_mfma_f32_16x16x32_bf16 v[70:73], v[146:149], v[186:189], v[70:73]
	v_mfma_f32_16x16x32_bf16 v[66:69], v[154:157], v[186:189], v[66:69]
	v_mfma_f32_16x16x32_bf16 v[118:121], v[150:153], v[166:169], v[118:121]
	v_mfma_f32_16x16x32_bf16 v[114:117], v[158:161], v[166:169], v[114:117]
	v_mfma_f32_16x16x32_bf16 v[102:105], v[150:153], v[174:177], v[102:105]
	v_mfma_f32_16x16x32_bf16 v[94:97], v[158:161], v[174:177], v[94:97]
	v_mfma_f32_16x16x32_bf16 v[86:89], v[150:153], v[182:185], v[86:89]
	v_mfma_f32_16x16x32_bf16 v[78:81], v[158:161], v[182:185], v[78:81]
	v_mfma_f32_16x16x32_bf16 v[70:73], v[150:153], v[206:209], v[70:73]
	v_mfma_f32_16x16x32_bf16 v[66:69], v[158:161], v[206:209], v[66:69]
	s_setprio 0
	s_barrier
	s_add_i32 s69, s69, s59
	v_lshl_add_u64 v[210:211], s[52:53], 0, v[0:1]
	s_mov_b32 m0, s69
	ds_read_b128 v[162:165], v234 offset:16384
	ds_read_b128 v[166:169], v234 offset:17408
	ds_read_b128 v[170:173], v234 offset:18432
	ds_read_b128 v[174:177], v234 offset:19456
	ds_read_b128 v[178:181], v234 offset:20480
	ds_read_b128 v[182:185], v234 offset:21504
	ds_read_b128 v[186:189], v234 offset:22528
	ds_read_b128 v[206:209], v234 offset:23552
	global_load_lds_dwordx4 v[210:211], off
	s_add_i32 m0, s69, 0x2000
	s_add_u32 s70, s52, 0x40000
	v_lshl_add_u64 v[212:213], s[52:53], 0, v[200:201]
	s_addc_u32 s71, s53, 0
	s_add_i32 s4, s4, s59
	global_load_lds_dwordx4 v[212:213], off
	v_lshl_add_u64 v[214:215], s[70:71], 0, v[0:1]
	s_mov_b32 m0, s4
	v_lshl_add_u64 v[216:217], s[54:55], 0, v[198:199]
	global_load_lds_dwordx4 v[214:215], off
	v_lshl_add_u64 v[214:215], s[70:71], 0, v[200:201]
	s_add_i32 m0, s4, 0x2000
	s_nop 0
	global_load_lds_dwordx4 v[214:215], off
	v_lshl_add_u64 v[214:215], s[54:55], 0, v[196:197]
	s_mov_b32 m0, s49
	s_nop 0
	global_load_lds_dwordx4 v[214:215], off
	s_mov_b32 m0, s30
	s_nop 0
	global_load_lds_dwordx4 v[216:217], off
	s_waitcnt vmcnt(8)
	s_waitcnt lgkmcnt(0)
	s_barrier
	s_setprio 1
	s_waitcnt lgkmcnt(0)
	v_mfma_f32_16x16x32_bf16 v[62:65], v[130:133], v[162:165], v[62:65]
	v_mfma_f32_16x16x32_bf16 v[58:61], v[138:141], v[162:165], v[58:61]
	v_mfma_f32_16x16x32_bf16 v[50:53], v[130:133], v[170:173], v[50:53]
	v_mfma_f32_16x16x32_bf16 v[42:45], v[138:141], v[170:173], v[42:45]
	v_mfma_f32_16x16x32_bf16 v[34:37], v[130:133], v[178:181], v[34:37]
	v_mfma_f32_16x16x32_bf16 v[26:29], v[138:141], v[178:181], v[26:29]
	v_mfma_f32_16x16x32_bf16 v[18:21], v[130:133], v[186:189], v[18:21]
	v_mfma_f32_16x16x32_bf16 v[10:13], v[138:141], v[186:189], v[10:13]
	v_mfma_f32_16x16x32_bf16 v[62:65], v[134:137], v[166:169], v[62:65]
	v_mfma_f32_16x16x32_bf16 v[58:61], v[142:145], v[166:169], v[58:61]
	v_mfma_f32_16x16x32_bf16 v[50:53], v[134:137], v[174:177], v[50:53]
	v_mfma_f32_16x16x32_bf16 v[42:45], v[142:145], v[174:177], v[42:45]
	v_mfma_f32_16x16x32_bf16 v[34:37], v[134:137], v[182:185], v[34:37]
	v_mfma_f32_16x16x32_bf16 v[26:29], v[142:145], v[182:185], v[26:29]
	v_mfma_f32_16x16x32_bf16 v[18:21], v[134:137], v[206:209], v[18:21]
	v_mfma_f32_16x16x32_bf16 v[10:13], v[142:145], v[206:209], v[10:13]
	v_mfma_f32_16x16x32_bf16 v[54:57], v[146:149], v[162:165], v[54:57]
	v_mfma_f32_16x16x32_bf16 v[46:49], v[154:157], v[162:165], v[46:49]
	v_mfma_f32_16x16x32_bf16 v[38:41], v[146:149], v[170:173], v[38:41]
	v_mfma_f32_16x16x32_bf16 v[30:33], v[154:157], v[170:173], v[30:33]
	v_mfma_f32_16x16x32_bf16 v[22:25], v[146:149], v[178:181], v[22:25]
	v_mfma_f32_16x16x32_bf16 v[14:17], v[154:157], v[178:181], v[14:17]
	v_mfma_f32_16x16x32_bf16 v[6:9], v[146:149], v[186:189], v[6:9]
	v_mfma_f32_16x16x32_bf16 v[2:5], v[154:157], v[186:189], v[2:5]
	v_mfma_f32_16x16x32_bf16 v[54:57], v[150:153], v[166:169], v[54:57]
	v_mfma_f32_16x16x32_bf16 v[46:49], v[158:161], v[166:169], v[46:49]
	v_mfma_f32_16x16x32_bf16 v[38:41], v[150:153], v[174:177], v[38:41]
	v_mfma_f32_16x16x32_bf16 v[30:33], v[158:161], v[174:177], v[30:33]
	v_mfma_f32_16x16x32_bf16 v[22:25], v[150:153], v[182:185], v[22:25]
	v_mfma_f32_16x16x32_bf16 v[14:17], v[158:161], v[182:185], v[14:17]
	v_mfma_f32_16x16x32_bf16 v[6:9], v[150:153], v[206:209], v[6:9]
	v_mfma_f32_16x16x32_bf16 v[2:5], v[158:161], v[206:209], v[2:5]
	s_setprio 0
	s_barrier
	s_add_i32 s4, 0, 0x18000
	s_add_i32 s69, 0, 0x1c000
	v_add_u32_e32 v142, s4, v195
	v_add_u32_e32 v158, s69, v195
	ds_read_b128 v[130:133], v142
	ds_read_b128 v[134:137], v142 offset:1024
	ds_read_b128 v[138:141], v142 offset:2048
	ds_read_b128 v[142:145], v142 offset:3072
	ds_read_b128 v[146:149], v158
	ds_read_b128 v[150:153], v158 offset:1024
	ds_read_b128 v[154:157], v158 offset:2048
	ds_read_b128 v[158:161], v158 offset:3072
	s_add_u32 s54, s54, 0x40000
	s_addc_u32 s55, s55, 0
	s_mov_b32 m0, s31
	v_lshl_add_u64 v[218:219], s[54:55], 0, v[196:197]
	ds_read_b128 v[162:165], v234 offset:32768
	ds_read_b128 v[166:169], v234 offset:33792
	ds_read_b128 v[170:173], v234 offset:34816
	ds_read_b128 v[174:177], v234 offset:35840
	ds_read_b128 v[178:181], v234 offset:36864
	ds_read_b128 v[182:185], v234 offset:37888
	ds_read_b128 v[186:189], v234 offset:38912
	ds_read_b128 v[206:209], v234 offset:39936
	global_load_lds_dwordx4 v[218:219], off
	v_lshl_add_u64 v[218:219], s[54:55], 0, v[198:199]
	s_mov_b32 m0, s60
	s_nop 0
	global_load_lds_dwordx4 v[218:219], off
	s_waitcnt vmcnt(8)
	s_waitcnt lgkmcnt(0)
	s_barrier
	s_setprio 1
	s_waitcnt lgkmcnt(0)
	v_mfma_f32_16x16x32_bf16 v[126:129], v[130:133], v[162:165], v[126:129]
	v_mfma_f32_16x16x32_bf16 v[122:125], v[138:141], v[162:165], v[122:125]
	v_mfma_f32_16x16x32_bf16 v[110:113], v[130:133], v[170:173], v[110:113]
	v_mfma_f32_16x16x32_bf16 v[106:109], v[138:141], v[170:173], v[106:109]
	v_mfma_f32_16x16x32_bf16 v[98:101], v[130:133], v[178:181], v[98:101]
	v_mfma_f32_16x16x32_bf16 v[90:93], v[138:141], v[178:181], v[90:93]
	v_mfma_f32_16x16x32_bf16 v[82:85], v[130:133], v[186:189], v[82:85]
	v_mfma_f32_16x16x32_bf16 v[74:77], v[138:141], v[186:189], v[74:77]
	v_mfma_f32_16x16x32_bf16 v[126:129], v[134:137], v[166:169], v[126:129]
	v_mfma_f32_16x16x32_bf16 v[122:125], v[142:145], v[166:169], v[122:125]
	v_mfma_f32_16x16x32_bf16 v[110:113], v[134:137], v[174:177], v[110:113]
	v_mfma_f32_16x16x32_bf16 v[106:109], v[142:145], v[174:177], v[106:109]
	v_mfma_f32_16x16x32_bf16 v[98:101], v[134:137], v[182:185], v[98:101]
	v_mfma_f32_16x16x32_bf16 v[90:93], v[142:145], v[182:185], v[90:93]
	v_mfma_f32_16x16x32_bf16 v[82:85], v[134:137], v[206:209], v[82:85]
	v_mfma_f32_16x16x32_bf16 v[74:77], v[142:145], v[206:209], v[74:77]
	v_mfma_f32_16x16x32_bf16 v[118:121], v[146:149], v[162:165], v[118:121]
	v_mfma_f32_16x16x32_bf16 v[114:117], v[154:157], v[162:165], v[114:117]
	v_mfma_f32_16x16x32_bf16 v[102:105], v[146:149], v[170:173], v[102:105]
	v_mfma_f32_16x16x32_bf16 v[94:97], v[154:157], v[170:173], v[94:97]
	v_mfma_f32_16x16x32_bf16 v[86:89], v[146:149], v[178:181], v[86:89]
	v_mfma_f32_16x16x32_bf16 v[78:81], v[154:157], v[178:181], v[78:81]
	v_mfma_f32_16x16x32_bf16 v[70:73], v[146:149], v[186:189], v[70:73]
	v_mfma_f32_16x16x32_bf16 v[66:69], v[154:157], v[186:189], v[66:69]
	v_mfma_f32_16x16x32_bf16 v[118:121], v[150:153], v[166:169], v[118:121]
	v_mfma_f32_16x16x32_bf16 v[114:117], v[158:161], v[166:169], v[114:117]
	v_mfma_f32_16x16x32_bf16 v[102:105], v[150:153], v[174:177], v[102:105]
	v_mfma_f32_16x16x32_bf16 v[94:97], v[158:161], v[174:177], v[94:97]
	v_mfma_f32_16x16x32_bf16 v[86:89], v[150:153], v[182:185], v[86:89]
	v_mfma_f32_16x16x32_bf16 v[78:81], v[158:161], v[182:185], v[78:81]
	v_mfma_f32_16x16x32_bf16 v[70:73], v[150:153], v[206:209], v[70:73]
	v_mfma_f32_16x16x32_bf16 v[66:69], v[158:161], v[206:209], v[66:69]
	s_setprio 0
	s_barrier
	s_add_i32 s4, s4, s59
	v_lshl_add_u64 v[210:211], v[210:211], 0, s[22:23]
	s_mov_b32 m0, s4
	ds_read_b128 v[162:165], v234 offset:49152
	ds_read_b128 v[166:169], v234 offset:50176
	ds_read_b128 v[170:173], v234 offset:51200
	ds_read_b128 v[174:177], v234 offset:52224
	ds_read_b128 v[178:181], v234 offset:53248
	ds_read_b128 v[182:185], v234 offset:54272
	ds_read_b128 v[186:189], v234 offset:55296
	ds_read_b128 v[206:209], v234 offset:56320
	global_load_lds_dwordx4 v[210:211], off
	s_add_i32 m0, s4, 0x2000
	s_add_u32 s52, s52, 0x40080
	v_lshl_add_u64 v[210:211], v[212:213], 0, s[22:23]
	s_addc_u32 s53, s53, 0
	s_add_i32 s4, s69, s59
	global_load_lds_dwordx4 v[210:211], off
	v_lshl_add_u64 v[210:211], s[52:53], 0, v[0:1]
	s_mov_b32 m0, s4
	s_nop 0
	global_load_lds_dwordx4 v[210:211], off
	v_lshl_add_u64 v[210:211], s[52:53], 0, v[200:201]
	s_add_i32 m0, s4, 0x2000
	s_nop 0
	global_load_lds_dwordx4 v[210:211], off
	v_lshl_add_u64 v[210:211], v[214:215], 0, s[22:23]
	s_mov_b32 m0, s62
	s_nop 0
	global_load_lds_dwordx4 v[210:211], off
	v_lshl_add_u64 v[210:211], v[216:217], 0, s[22:23]
	s_mov_b32 m0, s63
	s_nop 0
	global_load_lds_dwordx4 v[210:211], off
	s_waitcnt vmcnt(8)
	s_waitcnt lgkmcnt(0)
	s_barrier
	s_setprio 1
	s_waitcnt lgkmcnt(0)
	v_mfma_f32_16x16x32_bf16 v[62:65], v[130:133], v[162:165], v[62:65]
	v_mfma_f32_16x16x32_bf16 v[58:61], v[138:141], v[162:165], v[58:61]
	v_mfma_f32_16x16x32_bf16 v[50:53], v[130:133], v[170:173], v[50:53]
	v_mfma_f32_16x16x32_bf16 v[42:45], v[138:141], v[170:173], v[42:45]
	v_mfma_f32_16x16x32_bf16 v[34:37], v[130:133], v[178:181], v[34:37]
	v_mfma_f32_16x16x32_bf16 v[26:29], v[138:141], v[178:181], v[26:29]
	v_mfma_f32_16x16x32_bf16 v[18:21], v[130:133], v[186:189], v[18:21]
	v_mfma_f32_16x16x32_bf16 v[10:13], v[138:141], v[186:189], v[10:13]
	v_mfma_f32_16x16x32_bf16 v[62:65], v[134:137], v[166:169], v[62:65]
	v_mfma_f32_16x16x32_bf16 v[58:61], v[142:145], v[166:169], v[58:61]
	v_mfma_f32_16x16x32_bf16 v[50:53], v[134:137], v[174:177], v[50:53]
	v_mfma_f32_16x16x32_bf16 v[42:45], v[142:145], v[174:177], v[42:45]
	v_mfma_f32_16x16x32_bf16 v[34:37], v[134:137], v[182:185], v[34:37]
	v_mfma_f32_16x16x32_bf16 v[26:29], v[142:145], v[182:185], v[26:29]
	v_mfma_f32_16x16x32_bf16 v[18:21], v[134:137], v[206:209], v[18:21]
	v_mfma_f32_16x16x32_bf16 v[10:13], v[142:145], v[206:209], v[10:13]
	v_mfma_f32_16x16x32_bf16 v[54:57], v[146:149], v[162:165], v[54:57]
	v_mfma_f32_16x16x32_bf16 v[46:49], v[154:157], v[162:165], v[46:49]
	v_mfma_f32_16x16x32_bf16 v[38:41], v[146:149], v[170:173], v[38:41]
	v_mfma_f32_16x16x32_bf16 v[30:33], v[154:157], v[170:173], v[30:33]
	v_mfma_f32_16x16x32_bf16 v[22:25], v[146:149], v[178:181], v[22:25]
	v_mfma_f32_16x16x32_bf16 v[14:17], v[154:157], v[178:181], v[14:17]
	v_mfma_f32_16x16x32_bf16 v[6:9], v[146:149], v[186:189], v[6:9]
	v_mfma_f32_16x16x32_bf16 v[2:5], v[154:157], v[186:189], v[2:5]
	v_mfma_f32_16x16x32_bf16 v[54:57], v[150:153], v[166:169], v[54:57]
	v_mfma_f32_16x16x32_bf16 v[46:49], v[158:161], v[166:169], v[46:49]
	v_mfma_f32_16x16x32_bf16 v[38:41], v[150:153], v[174:177], v[38:41]
	v_mfma_f32_16x16x32_bf16 v[30:33], v[158:161], v[174:177], v[30:33]
	v_mfma_f32_16x16x32_bf16 v[22:25], v[150:153], v[182:185], v[22:25]
	v_mfma_f32_16x16x32_bf16 v[14:17], v[158:161], v[182:185], v[14:17]
	v_mfma_f32_16x16x32_bf16 v[6:9], v[150:153], v[206:209], v[6:9]
	v_mfma_f32_16x16x32_bf16 v[2:5], v[158:161], v[206:209], v[2:5]
	s_setprio 0
	s_barrier
	s_add_i32 s68, s68, 2
	s_add_u32 s50, s50, 0x100
	s_addc_u32 s51, s51, 0
	s_add_u32 s66, s66, 0x100
	s_addc_u32 s67, s67, 0
	s_cmp_gt_u32 s68, 13
	s_cbranch_scc0 .LBB0_508
	v_lshl_or_b32 v132, s6, 8, v233
	v_lshl_add_u32 v130, s48, 8, v193
	v_ashrrev_i32_e32 v133, 31, v132
	v_lshlrev_b64 v[206:207], 1, v[132:133]
	v_ashrrev_i32_e32 v131, 31, v130
	v_lshl_add_u64 v[132:133], s[40:41], 0, v[206:207]
	v_lshlrev_b64 v[222:223], 11, v[130:131]
	v_lshl_add_u64 v[134:135], v[132:133], 0, v[222:223]
	global_load_dwordx4 v[236:239], v[134:135], off nt
	global_load_dwordx4 v[186:189], v[134:135], off offset:256 nt
	v_or_b32_e32 v134, 16, v130
	v_ashrrev_i32_e32 v135, 31, v134
	v_lshlrev_b64 v[220:221], 11, v[134:135]
	v_lshl_add_u64 v[134:135], v[132:133], 0, v[220:221]
	global_load_dwordx4 v[182:185], v[134:135], off nt
	global_load_dwordx4 v[178:181], v[134:135], off offset:256 nt
	v_or_b32_e32 v134, 32, v130
	v_ashrrev_i32_e32 v135, 31, v134
	v_lshlrev_b64 v[218:219], 11, v[134:135]
	v_lshl_add_u64 v[134:135], v[132:133], 0, v[218:219]
	global_load_dwordx4 v[174:177], v[134:135], off nt
	global_load_dwordx4 v[170:173], v[134:135], off offset:256 nt
	v_or_b32_e32 v130, 48, v130
	v_ashrrev_i32_e32 v131, 31, v130
	v_lshlrev_b64 v[216:217], 11, v[130:131]
	v_lshl_add_u64 v[130:131], v[132:133], 0, v[216:217]
	global_load_dwordx4 v[166:169], v[130:131], off nt
	global_load_dwordx4 v[158:161], v[130:131], off offset:256 nt
	s_mov_b64 s[50:51], 0x40000
	v_lshl_add_u64 v[214:215], v[222:223], 0, s[50:51]
	v_lshl_add_u64 v[130:131], v[132:133], 0, v[214:215]
	global_load_dwordx4 v[162:165], v[130:131], off nt
	global_load_dwordx4 v[154:157], v[130:131], off offset:256 nt
	s_mov_b64 s[50:51], 0x48000
	v_lshl_add_u64 v[212:213], v[222:223], 0, s[50:51]
	v_lshl_add_u64 v[130:131], v[132:133], 0, v[212:213]
	global_load_dwordx4 v[150:153], v[130:131], off nt
	global_load_dwordx4 v[146:149], v[130:131], off offset:256 nt
	s_mov_b64 s[50:51], 0x50000
	v_lshl_add_u64 v[210:211], v[222:223], 0, s[50:51]
	v_lshl_add_u64 v[130:131], v[132:133], 0, v[210:211]
	global_load_dwordx4 v[142:145], v[130:131], off nt
	global_load_dwordx4 v[134:137], v[130:131], off offset:256 nt
	s_mov_b64 s[50:51], 0x58000
	v_lshl_add_u64 v[208:209], v[222:223], 0, s[50:51]
	v_lshl_add_u64 v[130:131], v[132:133], 0, v[208:209]
	global_load_dwordx4 v[138:141], v[130:131], off nt
	s_nop 0
	global_load_dwordx4 v[130:133], v[130:131], off offset:256 nt
	s_and_b64 vcc, exec, s[38:39]
	s_mov_b32 s6, s44
	s_mov_b32 s48, s46
	s_mov_b64 s[52:53], s[36:37]
	s_mov_b64 s[50:51], s[26:27]
	s_waitcnt vmcnt(0)
	v_lshlrev_b32_e32 v230, 16, v236
	v_and_b32_e32 v231, 0xffff0000, v236
	v_lshlrev_b32_e32 v236, 16, v237
	v_and_b32_e32 v237, 0xffff0000, v237
	v_pk_add_f32 v[128:129], v[128:129], v[236:237]
	v_pk_add_f32 v[126:127], v[126:127], v[230:231]
	v_lshlrev_b32_e32 v230, 16, v238
	v_and_b32_e32 v231, 0xffff0000, v238
	v_lshlrev_b32_e32 v236, 16, v239
	v_and_b32_e32 v237, 0xffff0000, v239
	v_pk_add_f32 v[236:237], v[124:125], v[236:237]
	v_pk_add_f32 v[124:125], v[122:123], v[230:231]
	v_cvt_pk_bf16_f32 v122, v126, v127
	v_lshl_add_u64 v[126:127], s[42:43], 0, v[222:223]
	v_cvt_pk_bf16_f32 v123, v128, v129
	v_cvt_pk_bf16_f32 v124, v124, v125
	v_cvt_pk_bf16_f32 v125, v236, v237
	v_lshl_add_u64 v[126:127], v[126:127], 0, v[206:207]
	global_store_dwordx4 v[126:127], v[122:125], off
	s_nop 1
	v_lshlrev_b32_e32 v122, 16, v186
	v_and_b32_e32 v123, 0xffff0000, v186
	v_lshlrev_b32_e32 v124, 16, v187
	v_and_b32_e32 v125, 0xffff0000, v187
	v_pk_add_f32 v[120:121], v[120:121], v[124:125]
	v_pk_add_f32 v[118:119], v[118:119], v[122:123]
	v_lshlrev_b32_e32 v122, 16, v188
	v_and_b32_e32 v123, 0xffff0000, v188
	v_lshlrev_b32_e32 v124, 16, v189
	v_and_b32_e32 v125, 0xffff0000, v189
	v_pk_add_f32 v[124:125], v[116:117], v[124:125]
	v_pk_add_f32 v[116:117], v[114:115], v[122:123]
	v_cvt_pk_bf16_f32 v114, v118, v119
	v_cvt_pk_bf16_f32 v115, v120, v121
	v_cvt_pk_bf16_f32 v116, v116, v117
	v_cvt_pk_bf16_f32 v117, v124, v125
	global_store_dwordx4 v[126:127], v[114:117], off offset:256
	s_nop 1
	v_lshlrev_b32_e32 v114, 16, v182
	v_and_b32_e32 v115, 0xffff0000, v182
	v_lshlrev_b32_e32 v116, 16, v183
	v_and_b32_e32 v117, 0xffff0000, v183
	v_pk_add_f32 v[112:113], v[112:113], v[116:117]
	v_pk_add_f32 v[110:111], v[110:111], v[114:115]
	v_lshlrev_b32_e32 v114, 16, v184
	v_and_b32_e32 v115, 0xffff0000, v184
	v_lshlrev_b32_e32 v116, 16, v185
	v_and_b32_e32 v117, 0xffff0000, v185
	v_pk_add_f32 v[116:117], v[108:109], v[116:117]
	v_pk_add_f32 v[108:109], v[106:107], v[114:115]
	v_cvt_pk_bf16_f32 v106, v110, v111
	v_lshl_add_u64 v[110:111], s[42:43], 0, v[220:221]
	v_cvt_pk_bf16_f32 v107, v112, v113
	v_cvt_pk_bf16_f32 v108, v108, v109
	v_cvt_pk_bf16_f32 v109, v116, v117
	v_lshl_add_u64 v[110:111], v[110:111], 0, v[206:207]
	global_store_dwordx4 v[110:111], v[106:109], off
	s_nop 1
	v_lshlrev_b32_e32 v106, 16, v178
	v_and_b32_e32 v107, 0xffff0000, v178
	v_lshlrev_b32_e32 v108, 16, v179
	v_and_b32_e32 v109, 0xffff0000, v179
	v_pk_add_f32 v[104:105], v[104:105], v[108:109]
	v_pk_add_f32 v[102:103], v[102:103], v[106:107]
	v_lshlrev_b32_e32 v106, 16, v180
	v_and_b32_e32 v107, 0xffff0000, v180
	v_lshlrev_b32_e32 v108, 16, v181
	v_and_b32_e32 v109, 0xffff0000, v181
	v_pk_add_f32 v[108:109], v[96:97], v[108:109]
	v_pk_add_f32 v[96:97], v[94:95], v[106:107]
	v_cvt_pk_bf16_f32 v94, v102, v103
	v_cvt_pk_bf16_f32 v95, v104, v105
	v_cvt_pk_bf16_f32 v96, v96, v97
	v_cvt_pk_bf16_f32 v97, v108, v109
	global_store_dwordx4 v[110:111], v[94:97], off offset:256
	s_nop 1
	v_lshlrev_b32_e32 v94, 16, v174
	v_and_b32_e32 v95, 0xffff0000, v174
	v_lshlrev_b32_e32 v96, 16, v175
	v_and_b32_e32 v97, 0xffff0000, v175
	v_pk_add_f32 v[96:97], v[100:101], v[96:97]
	v_pk_add_f32 v[94:95], v[98:99], v[94:95]
	v_lshlrev_b32_e32 v98, 16, v176
	v_and_b32_e32 v99, 0xffff0000, v176
	v_lshlrev_b32_e32 v100, 16, v177
	v_and_b32_e32 v101, 0xffff0000, v177
	v_pk_add_f32 v[100:101], v[92:93], v[100:101]
	v_pk_add_f32 v[92:93], v[90:91], v[98:99]
	v_cvt_pk_bf16_f32 v90, v94, v95
	v_lshl_add_u64 v[94:95], s[42:43], 0, v[218:219]
	v_cvt_pk_bf16_f32 v91, v96, v97
	v_cvt_pk_bf16_f32 v92, v92, v93
	v_cvt_pk_bf16_f32 v93, v100, v101
	v_lshl_add_u64 v[94:95], v[94:95], 0, v[206:207]
	global_store_dwordx4 v[94:95], v[90:93], off
	s_nop 1
	v_lshlrev_b32_e32 v90, 16, v170
	v_and_b32_e32 v91, 0xffff0000, v170
	v_lshlrev_b32_e32 v92, 16, v171
	v_and_b32_e32 v93, 0xffff0000, v171
	v_pk_add_f32 v[88:89], v[88:89], v[92:93]
	v_pk_add_f32 v[86:87], v[86:87], v[90:91]
	v_lshlrev_b32_e32 v90, 16, v172
	v_and_b32_e32 v91, 0xffff0000, v172
	v_lshlrev_b32_e32 v92, 16, v173
	v_and_b32_e32 v93, 0xffff0000, v173
	v_pk_add_f32 v[92:93], v[80:81], v[92:93]
	v_pk_add_f32 v[80:81], v[78:79], v[90:91]
	v_cvt_pk_bf16_f32 v78, v86, v87
	v_cvt_pk_bf16_f32 v79, v88, v89
	v_cvt_pk_bf16_f32 v80, v80, v81
	v_cvt_pk_bf16_f32 v81, v92, v93
	global_store_dwordx4 v[94:95], v[78:81], off offset:256
	s_nop 1
	v_lshlrev_b32_e32 v78, 16, v166
	v_and_b32_e32 v79, 0xffff0000, v166
	v_lshlrev_b32_e32 v80, 16, v167
	v_and_b32_e32 v81, 0xffff0000, v167
	v_pk_add_f32 v[80:81], v[84:85], v[80:81]
	v_pk_add_f32 v[78:79], v[82:83], v[78:79]
	v_lshlrev_b32_e32 v82, 16, v168
	v_and_b32_e32 v83, 0xffff0000, v168
	v_lshlrev_b32_e32 v84, 16, v169
	v_and_b32_e32 v85, 0xffff0000, v169
	v_pk_add_f32 v[84:85], v[76:77], v[84:85]
	v_pk_add_f32 v[76:77], v[74:75], v[82:83]
	v_cvt_pk_bf16_f32 v74, v78, v79
	v_lshl_add_u64 v[78:79], s[42:43], 0, v[216:217]
	v_cvt_pk_bf16_f32 v75, v80, v81
	v_cvt_pk_bf16_f32 v76, v76, v77
	v_cvt_pk_bf16_f32 v77, v84, v85
	v_lshl_add_u64 v[78:79], v[78:79], 0, v[206:207]
	global_store_dwordx4 v[78:79], v[74:77], off
	s_nop 1
	v_lshlrev_b32_e32 v74, 16, v158
	v_and_b32_e32 v75, 0xffff0000, v158
	v_lshlrev_b32_e32 v76, 16, v159
	v_and_b32_e32 v77, 0xffff0000, v159
	v_pk_add_f32 v[72:73], v[72:73], v[76:77]
	v_pk_add_f32 v[70:71], v[70:71], v[74:75]
	v_lshlrev_b32_e32 v74, 16, v160
	v_and_b32_e32 v75, 0xffff0000, v160
	v_lshlrev_b32_e32 v76, 16, v161
	v_and_b32_e32 v77, 0xffff0000, v161
	v_pk_add_f32 v[76:77], v[68:69], v[76:77]
	v_pk_add_f32 v[68:69], v[66:67], v[74:75]
	v_cvt_pk_bf16_f32 v66, v70, v71
	v_cvt_pk_bf16_f32 v67, v72, v73
	v_cvt_pk_bf16_f32 v68, v68, v69
	v_cvt_pk_bf16_f32 v69, v76, v77
	global_store_dwordx4 v[78:79], v[66:69], off offset:256
	s_nop 1
	v_lshlrev_b32_e32 v66, 16, v162
	v_and_b32_e32 v67, 0xffff0000, v162
	v_lshlrev_b32_e32 v68, 16, v163
	v_and_b32_e32 v69, 0xffff0000, v163
	v_pk_add_f32 v[64:65], v[64:65], v[68:69]
	v_pk_add_f32 v[62:63], v[62:63], v[66:67]
	v_lshlrev_b32_e32 v66, 16, v164
	v_and_b32_e32 v67, 0xffff0000, v164
	v_lshlrev_b32_e32 v68, 16, v165
	v_and_b32_e32 v69, 0xffff0000, v165
	v_pk_add_f32 v[68:69], v[60:61], v[68:69]
	v_pk_add_f32 v[60:61], v[58:59], v[66:67]
	v_cvt_pk_bf16_f32 v58, v62, v63
	v_lshl_add_u64 v[62:63], s[42:43], 0, v[214:215]
	v_cvt_pk_bf16_f32 v59, v64, v65
	v_cvt_pk_bf16_f32 v60, v60, v61
	v_cvt_pk_bf16_f32 v61, v68, v69
	v_lshl_add_u64 v[62:63], v[62:63], 0, v[206:207]
	global_store_dwordx4 v[62:63], v[58:61], off
	s_nop 1
	v_lshlrev_b32_e32 v58, 16, v154
	v_and_b32_e32 v59, 0xffff0000, v154
	v_lshlrev_b32_e32 v60, 16, v155
	v_and_b32_e32 v61, 0xffff0000, v155
	v_pk_add_f32 v[56:57], v[56:57], v[60:61]
	v_pk_add_f32 v[54:55], v[54:55], v[58:59]
	v_lshlrev_b32_e32 v58, 16, v156
	v_and_b32_e32 v59, 0xffff0000, v156
	v_lshlrev_b32_e32 v60, 16, v157
	v_and_b32_e32 v61, 0xffff0000, v157
	v_pk_add_f32 v[60:61], v[48:49], v[60:61]
	v_pk_add_f32 v[48:49], v[46:47], v[58:59]
	v_cvt_pk_bf16_f32 v46, v54, v55
	v_cvt_pk_bf16_f32 v47, v56, v57
	v_cvt_pk_bf16_f32 v48, v48, v49
	v_cvt_pk_bf16_f32 v49, v60, v61
	global_store_dwordx4 v[62:63], v[46:49], off offset:256
	s_nop 1
	v_lshlrev_b32_e32 v46, 16, v150
	v_and_b32_e32 v47, 0xffff0000, v150
	v_lshlrev_b32_e32 v48, 16, v151
	v_and_b32_e32 v49, 0xffff0000, v151
	v_pk_add_f32 v[48:49], v[52:53], v[48:49]
	v_pk_add_f32 v[46:47], v[50:51], v[46:47]
	v_lshlrev_b32_e32 v50, 16, v152
	v_and_b32_e32 v51, 0xffff0000, v152
	v_lshlrev_b32_e32 v52, 16, v153
	v_and_b32_e32 v53, 0xffff0000, v153
	v_pk_add_f32 v[52:53], v[44:45], v[52:53]
	v_pk_add_f32 v[44:45], v[42:43], v[50:51]
	v_cvt_pk_bf16_f32 v42, v46, v47
	v_lshl_add_u64 v[46:47], s[42:43], 0, v[212:213]
	v_cvt_pk_bf16_f32 v43, v48, v49
	v_cvt_pk_bf16_f32 v44, v44, v45
	v_cvt_pk_bf16_f32 v45, v52, v53
	v_lshl_add_u64 v[46:47], v[46:47], 0, v[206:207]
	global_store_dwordx4 v[46:47], v[42:45], off
	s_nop 1
	v_lshlrev_b32_e32 v42, 16, v146
	v_and_b32_e32 v43, 0xffff0000, v146
	v_lshlrev_b32_e32 v44, 16, v147
	v_and_b32_e32 v45, 0xffff0000, v147
	v_pk_add_f32 v[40:41], v[40:41], v[44:45]
	v_pk_add_f32 v[38:39], v[38:39], v[42:43]
	v_lshlrev_b32_e32 v42, 16, v148
	v_and_b32_e32 v43, 0xffff0000, v148
	v_lshlrev_b32_e32 v44, 16, v149
	v_and_b32_e32 v45, 0xffff0000, v149
	v_pk_add_f32 v[44:45], v[32:33], v[44:45]
	v_pk_add_f32 v[32:33], v[30:31], v[42:43]
	v_cvt_pk_bf16_f32 v30, v38, v39
	v_cvt_pk_bf16_f32 v31, v40, v41
	v_cvt_pk_bf16_f32 v32, v32, v33
	v_cvt_pk_bf16_f32 v33, v44, v45
	global_store_dwordx4 v[46:47], v[30:33], off offset:256
	s_nop 1
	v_lshlrev_b32_e32 v30, 16, v142
	v_and_b32_e32 v31, 0xffff0000, v142
	v_lshlrev_b32_e32 v32, 16, v143
	v_and_b32_e32 v33, 0xffff0000, v143
	v_pk_add_f32 v[32:33], v[36:37], v[32:33]
	v_pk_add_f32 v[30:31], v[34:35], v[30:31]
	v_lshlrev_b32_e32 v34, 16, v144
	v_and_b32_e32 v35, 0xffff0000, v144
	v_lshlrev_b32_e32 v36, 16, v145
	v_and_b32_e32 v37, 0xffff0000, v145
	v_pk_add_f32 v[36:37], v[28:29], v[36:37]
	v_pk_add_f32 v[28:29], v[26:27], v[34:35]
	v_cvt_pk_bf16_f32 v26, v30, v31
	v_lshl_add_u64 v[30:31], s[42:43], 0, v[210:211]
	v_cvt_pk_bf16_f32 v27, v32, v33
	v_cvt_pk_bf16_f32 v28, v28, v29
	v_cvt_pk_bf16_f32 v29, v36, v37
	v_lshl_add_u64 v[30:31], v[30:31], 0, v[206:207]
	global_store_dwordx4 v[30:31], v[26:29], off
	s_nop 1
	v_lshlrev_b32_e32 v26, 16, v134
	v_and_b32_e32 v27, 0xffff0000, v134
	v_lshlrev_b32_e32 v28, 16, v135
	v_and_b32_e32 v29, 0xffff0000, v135
	v_pk_add_f32 v[24:25], v[24:25], v[28:29]
	v_pk_add_f32 v[22:23], v[22:23], v[26:27]
	v_lshlrev_b32_e32 v26, 16, v136
	v_and_b32_e32 v27, 0xffff0000, v136
	v_lshlrev_b32_e32 v28, 16, v137
	v_and_b32_e32 v29, 0xffff0000, v137
	v_pk_add_f32 v[28:29], v[16:17], v[28:29]
	v_pk_add_f32 v[16:17], v[14:15], v[26:27]
	v_cvt_pk_bf16_f32 v14, v22, v23
	v_cvt_pk_bf16_f32 v15, v24, v25
	v_cvt_pk_bf16_f32 v16, v16, v17
	v_cvt_pk_bf16_f32 v17, v28, v29
	global_store_dwordx4 v[30:31], v[14:17], off offset:256
	s_nop 1
	v_lshlrev_b32_e32 v14, 16, v138
	v_and_b32_e32 v15, 0xffff0000, v138
	v_lshlrev_b32_e32 v16, 16, v139
	v_and_b32_e32 v17, 0xffff0000, v139
	v_pk_add_f32 v[16:17], v[20:21], v[16:17]
	v_pk_add_f32 v[14:15], v[18:19], v[14:15]
	v_lshlrev_b32_e32 v18, 16, v140
	v_and_b32_e32 v19, 0xffff0000, v140
	v_lshlrev_b32_e32 v20, 16, v141
	v_and_b32_e32 v21, 0xffff0000, v141
	v_pk_add_f32 v[20:21], v[12:13], v[20:21]
	v_pk_add_f32 v[12:13], v[10:11], v[18:19]
	v_cvt_pk_bf16_f32 v10, v14, v15
	v_lshl_add_u64 v[14:15], s[42:43], 0, v[208:209]
	v_cvt_pk_bf16_f32 v11, v16, v17
	v_cvt_pk_bf16_f32 v12, v12, v13
	v_cvt_pk_bf16_f32 v13, v20, v21
	v_lshl_add_u64 v[14:15], v[14:15], 0, v[206:207]
	global_store_dwordx4 v[14:15], v[10:13], off
	s_nop 1
	v_lshlrev_b32_e32 v10, 16, v130
	v_and_b32_e32 v11, 0xffff0000, v130
	v_lshlrev_b32_e32 v12, 16, v131
	v_and_b32_e32 v13, 0xffff0000, v131
	v_pk_add_f32 v[8:9], v[8:9], v[12:13]
	v_pk_add_f32 v[6:7], v[6:7], v[10:11]
	v_lshlrev_b32_e32 v10, 16, v132
	v_and_b32_e32 v11, 0xffff0000, v132
	v_lshlrev_b32_e32 v12, 16, v133
	v_and_b32_e32 v13, 0xffff0000, v133
	v_pk_add_f32 v[12:13], v[4:5], v[12:13]
	v_pk_add_f32 v[4:5], v[2:3], v[10:11]
	v_cvt_pk_bf16_f32 v2, v6, v7
	v_cvt_pk_bf16_f32 v3, v8, v9
	v_cvt_pk_bf16_f32 v4, v4, v5
	v_cvt_pk_bf16_f32 v5, v12, v13
	global_store_dwordx4 v[14:15], v[2:5], off offset:256
	s_cbranch_vccz .LBB0_501
	s_waitcnt vmcnt(0)
	s_cmpk_gt_u32 s14, 0xff
	s_cbranch_scc1 .LBB0_512
	s_barrier

.LBB0_673:
	s_add_u32 s62, s36, 0xfffc0080
	s_addc_u32 s63, s37, -1
	s_add_i32 s86, 0, 0x10000
	s_cmp_eq_u32 s85, 12
	s_cselect_b32 s65, s6, s63
	s_cselect_b32 s64, s27, s62
	v_add_u32_e32 v0, s86, v208
	s_cselect_b32 s63, s55, s84
	s_cselect_b32 s62, s57, s74
	s_add_i32 s87, 0, 0x14000
	ds_read_b128 v[130:133], v0
	ds_read_b128 v[134:137], v0 offset:1024
	ds_read_b128 v[138:141], v0 offset:2048
	ds_read_b128 v[142:145], v0 offset:3072
	v_add_u32_e32 v0, s87, v208
	ds_read_b128 v[146:149], v0
	ds_read_b128 v[150:153], v0 offset:1024
	ds_read_b128 v[154:157], v0 offset:2048
	ds_read_b128 v[158:161], v0 offset:3072
	v_lshl_add_u64 v[202:203], s[36:37], 0, v[172:173]
	s_add_i32 m0, s68, 0xc000
	ds_read_b128 v[184:187], v210
	ds_read_b128 v[198:201], v210 offset:1024
	ds_read_b128 v[212:215], v210 offset:2048
	ds_read_b128 v[216:219], v210 offset:3072
	ds_read_b128 v[220:223], v210 offset:4096
	ds_read_b128 v[234:237], v210 offset:5120
	ds_read_b128 v[238:241], v210 offset:6144
	ds_read_b128 v[242:245], v210 offset:7168
	global_load_lds_dwordx4 v[202:203], off
	v_lshl_add_u64 v[202:203], s[36:37], 0, v[174:175]
	s_add_i32 m0, s68, 0xe000
	s_nop 0
	global_load_lds_dwordx4 v[202:203], off
	s_waitcnt vmcnt(8)
	s_waitcnt lgkmcnt(0)
	s_barrier
	s_setprio 1
	s_waitcnt lgkmcnt(0)
	v_mfma_f32_16x16x32_bf16 v[126:129], v[130:133], v[184:187], v[126:129]
	v_mfma_f32_16x16x32_bf16 v[122:125], v[138:141], v[184:187], v[122:125]
	v_mfma_f32_16x16x32_bf16 v[118:121], v[130:133], v[212:215], v[118:121]
	v_mfma_f32_16x16x32_bf16 v[114:117], v[138:141], v[212:215], v[114:117]
	v_mfma_f32_16x16x32_bf16 v[94:97], v[130:133], v[220:223], v[94:97]
	v_mfma_f32_16x16x32_bf16 v[90:93], v[138:141], v[220:223], v[90:93]
	v_mfma_f32_16x16x32_bf16 v[86:89], v[130:133], v[238:241], v[86:89]
	v_mfma_f32_16x16x32_bf16 v[82:85], v[138:141], v[238:241], v[82:85]
	v_mfma_f32_16x16x32_bf16 v[126:129], v[134:137], v[198:201], v[126:129]
	v_mfma_f32_16x16x32_bf16 v[122:125], v[142:145], v[198:201], v[122:125]
	v_mfma_f32_16x16x32_bf16 v[118:121], v[134:137], v[216:219], v[118:121]
	v_mfma_f32_16x16x32_bf16 v[114:117], v[142:145], v[216:219], v[114:117]
	v_mfma_f32_16x16x32_bf16 v[94:97], v[134:137], v[234:237], v[94:97]
	v_mfma_f32_16x16x32_bf16 v[90:93], v[142:145], v[234:237], v[90:93]
	v_mfma_f32_16x16x32_bf16 v[86:89], v[134:137], v[242:245], v[86:89]
	v_mfma_f32_16x16x32_bf16 v[82:85], v[142:145], v[242:245], v[82:85]
	v_mfma_f32_16x16x32_bf16 v[110:113], v[146:149], v[184:187], v[110:113]
	v_mfma_f32_16x16x32_bf16 v[106:109], v[154:157], v[184:187], v[106:109]
	v_mfma_f32_16x16x32_bf16 v[102:105], v[146:149], v[212:215], v[102:105]
	v_mfma_f32_16x16x32_bf16 v[98:101], v[154:157], v[212:215], v[98:101]
	v_mfma_f32_16x16x32_bf16 v[78:81], v[146:149], v[220:223], v[78:81]
	v_mfma_f32_16x16x32_bf16 v[74:77], v[154:157], v[220:223], v[74:77]
	v_mfma_f32_16x16x32_bf16 v[70:73], v[146:149], v[238:241], v[70:73]
	v_mfma_f32_16x16x32_bf16 v[66:69], v[154:157], v[238:241], v[66:69]
	v_mfma_f32_16x16x32_bf16 v[110:113], v[150:153], v[198:201], v[110:113]
	v_mfma_f32_16x16x32_bf16 v[106:109], v[158:161], v[198:201], v[106:109]
	v_mfma_f32_16x16x32_bf16 v[102:105], v[150:153], v[216:219], v[102:105]
	v_mfma_f32_16x16x32_bf16 v[98:101], v[158:161], v[216:219], v[98:101]
	v_mfma_f32_16x16x32_bf16 v[78:81], v[150:153], v[234:237], v[78:81]
	v_mfma_f32_16x16x32_bf16 v[74:77], v[158:161], v[234:237], v[74:77]
	v_mfma_f32_16x16x32_bf16 v[70:73], v[150:153], v[242:245], v[70:73]
	v_mfma_f32_16x16x32_bf16 v[66:69], v[158:161], v[242:245], v[66:69]
	s_setprio 0
	s_barrier
	s_add_i32 s86, s86, s67
	v_lshl_add_u64 v[202:203], s[62:63], 0, v[166:167]
	s_mov_b32 m0, s86
	ds_read_b128 v[184:187], v210 offset:16384
	ds_read_b128 v[198:201], v210 offset:17408
	ds_read_b128 v[212:215], v210 offset:18432
	ds_read_b128 v[216:219], v210 offset:19456
	ds_read_b128 v[220:223], v210 offset:20480
	ds_read_b128 v[234:237], v210 offset:21504
	ds_read_b128 v[238:241], v210 offset:22528
	ds_read_b128 v[242:245], v210 offset:23552
	global_load_lds_dwordx4 v[202:203], off
	s_add_i32 m0, s86, 0x2000
	s_add_u32 s92, s62, 0x40000
	v_lshl_add_u64 v[246:247], s[62:63], 0, v[170:171]
	s_addc_u32 s93, s63, 0
	s_add_i32 s86, s87, s67
	global_load_lds_dwordx4 v[246:247], off
	v_lshl_add_u64 v[248:249], s[92:93], 0, v[166:167]
	s_mov_b32 m0, s86
	v_lshl_add_u64 v[250:251], s[64:65], 0, v[168:169]
	global_load_lds_dwordx4 v[248:249], off
	v_lshl_add_u64 v[248:249], s[92:93], 0, v[170:171]
	s_add_i32 m0, s86, 0x2000
	s_nop 0
	global_load_lds_dwordx4 v[248:249], off
	v_lshl_add_u64 v[248:249], s[64:65], 0, v[164:165]
	s_mov_b32 m0, s68
	s_nop 0
	global_load_lds_dwordx4 v[248:249], off
	s_mov_b32 m0, s69
	s_nop 0
	global_load_lds_dwordx4 v[250:251], off
	s_waitcnt vmcnt(8)
	s_waitcnt lgkmcnt(0)
	s_barrier
	s_setprio 1
	s_waitcnt lgkmcnt(0)
	v_mfma_f32_16x16x32_bf16 v[62:65], v[130:133], v[184:187], v[62:65]
	v_mfma_f32_16x16x32_bf16 v[58:61], v[138:141], v[184:187], v[58:61]
	v_mfma_f32_16x16x32_bf16 v[54:57], v[130:133], v[212:215], v[54:57]
	v_mfma_f32_16x16x32_bf16 v[50:53], v[138:141], v[212:215], v[50:53]
	v_mfma_f32_16x16x32_bf16 v[30:33], v[130:133], v[220:223], v[30:33]
	v_mfma_f32_16x16x32_bf16 v[26:29], v[138:141], v[220:223], v[26:29]
	v_mfma_f32_16x16x32_bf16 v[22:25], v[130:133], v[238:241], v[22:25]
	v_mfma_f32_16x16x32_bf16 v[18:21], v[138:141], v[238:241], v[18:21]
	v_mfma_f32_16x16x32_bf16 v[62:65], v[134:137], v[198:201], v[62:65]
	v_mfma_f32_16x16x32_bf16 v[58:61], v[142:145], v[198:201], v[58:61]
	v_mfma_f32_16x16x32_bf16 v[54:57], v[134:137], v[216:219], v[54:57]
	v_mfma_f32_16x16x32_bf16 v[50:53], v[142:145], v[216:219], v[50:53]
	v_mfma_f32_16x16x32_bf16 v[30:33], v[134:137], v[234:237], v[30:33]
	v_mfma_f32_16x16x32_bf16 v[26:29], v[142:145], v[234:237], v[26:29]
	v_mfma_f32_16x16x32_bf16 v[22:25], v[134:137], v[242:245], v[22:25]
	v_mfma_f32_16x16x32_bf16 v[18:21], v[142:145], v[242:245], v[18:21]
	v_mfma_f32_16x16x32_bf16 v[46:49], v[146:149], v[184:187], v[46:49]
	v_mfma_f32_16x16x32_bf16 v[42:45], v[154:157], v[184:187], v[42:45]
	v_mfma_f32_16x16x32_bf16 v[38:41], v[146:149], v[212:215], v[38:41]
	v_mfma_f32_16x16x32_bf16 v[34:37], v[154:157], v[212:215], v[34:37]
	v_mfma_f32_16x16x32_bf16 v[14:17], v[146:149], v[220:223], v[14:17]
	v_mfma_f32_16x16x32_bf16 v[10:13], v[154:157], v[220:223], v[10:13]
	v_mfma_f32_16x16x32_bf16 v[6:9], v[146:149], v[238:241], v[6:9]
	v_mfma_f32_16x16x32_bf16 v[2:5], v[154:157], v[238:241], v[2:5]
	v_mfma_f32_16x16x32_bf16 v[46:49], v[150:153], v[198:201], v[46:49]
	v_mfma_f32_16x16x32_bf16 v[42:45], v[158:161], v[198:201], v[42:45]
	v_mfma_f32_16x16x32_bf16 v[38:41], v[150:153], v[216:219], v[38:41]
	v_mfma_f32_16x16x32_bf16 v[34:37], v[158:161], v[216:219], v[34:37]
	v_mfma_f32_16x16x32_bf16 v[14:17], v[150:153], v[234:237], v[14:17]
	v_mfma_f32_16x16x32_bf16 v[10:13], v[158:161], v[234:237], v[10:13]
	v_mfma_f32_16x16x32_bf16 v[6:9], v[150:153], v[242:245], v[6:9]
	v_mfma_f32_16x16x32_bf16 v[2:5], v[158:161], v[242:245], v[2:5]
	s_setprio 0
	s_barrier
	s_add_i32 s86, 0, 0x18000
	v_add_u32_e32 v0, s86, v208
	s_add_i32 s87, 0, 0x1c000
	ds_read_b128 v[130:133], v0
	ds_read_b128 v[134:137], v0 offset:1024
	ds_read_b128 v[138:141], v0 offset:2048
	ds_read_b128 v[142:145], v0 offset:3072
	v_add_u32_e32 v0, s87, v208
	ds_read_b128 v[146:149], v0
	ds_read_b128 v[150:153], v0 offset:1024
	ds_read_b128 v[154:157], v0 offset:2048
	ds_read_b128 v[158:161], v0 offset:3072
	s_add_u32 s64, s64, 0x40000
	s_addc_u32 s65, s65, 0
	s_mov_b32 m0, s70
	v_lshl_add_u64 v[230:231], s[64:65], 0, v[164:165]
	ds_read_b128 v[184:187], v210 offset:32768
	ds_read_b128 v[198:201], v210 offset:33792
	ds_read_b128 v[212:215], v210 offset:34816
	ds_read_b128 v[216:219], v210 offset:35840
	ds_read_b128 v[220:223], v210 offset:36864
	ds_read_b128 v[234:237], v210 offset:37888
	ds_read_b128 v[238:241], v210 offset:38912
	ds_read_b128 v[242:245], v210 offset:39936
	global_load_lds_dwordx4 v[230:231], off
	v_lshl_add_u64 v[230:231], s[64:65], 0, v[168:169]
	s_mov_b32 m0, s71
	s_nop 0
	global_load_lds_dwordx4 v[230:231], off
	s_waitcnt vmcnt(8)
	s_waitcnt lgkmcnt(0)
	s_barrier
	s_setprio 1
	s_waitcnt lgkmcnt(0)
	v_mfma_f32_16x16x32_bf16 v[126:129], v[130:133], v[184:187], v[126:129]
	v_mfma_f32_16x16x32_bf16 v[122:125], v[138:141], v[184:187], v[122:125]
	v_mfma_f32_16x16x32_bf16 v[118:121], v[130:133], v[212:215], v[118:121]
	v_mfma_f32_16x16x32_bf16 v[114:117], v[138:141], v[212:215], v[114:117]
	v_mfma_f32_16x16x32_bf16 v[94:97], v[130:133], v[220:223], v[94:97]
	v_mfma_f32_16x16x32_bf16 v[90:93], v[138:141], v[220:223], v[90:93]
	v_mfma_f32_16x16x32_bf16 v[86:89], v[130:133], v[238:241], v[86:89]
	v_mfma_f32_16x16x32_bf16 v[82:85], v[138:141], v[238:241], v[82:85]
	v_mfma_f32_16x16x32_bf16 v[126:129], v[134:137], v[198:201], v[126:129]
	v_mfma_f32_16x16x32_bf16 v[122:125], v[142:145], v[198:201], v[122:125]
	v_mfma_f32_16x16x32_bf16 v[118:121], v[134:137], v[216:219], v[118:121]
	v_mfma_f32_16x16x32_bf16 v[114:117], v[142:145], v[216:219], v[114:117]
	v_mfma_f32_16x16x32_bf16 v[94:97], v[134:137], v[234:237], v[94:97]
	v_mfma_f32_16x16x32_bf16 v[90:93], v[142:145], v[234:237], v[90:93]
	v_mfma_f32_16x16x32_bf16 v[86:89], v[134:137], v[242:245], v[86:89]
	v_mfma_f32_16x16x32_bf16 v[82:85], v[142:145], v[242:245], v[82:85]
	v_mfma_f32_16x16x32_bf16 v[110:113], v[146:149], v[184:187], v[110:113]
	v_mfma_f32_16x16x32_bf16 v[106:109], v[154:157], v[184:187], v[106:109]
	v_mfma_f32_16x16x32_bf16 v[102:105], v[146:149], v[212:215], v[102:105]
	v_mfma_f32_16x16x32_bf16 v[98:101], v[154:157], v[212:215], v[98:101]
	v_mfma_f32_16x16x32_bf16 v[78:81], v[146:149], v[220:223], v[78:81]
	v_mfma_f32_16x16x32_bf16 v[74:77], v[154:157], v[220:223], v[74:77]
	v_mfma_f32_16x16x32_bf16 v[70:73], v[146:149], v[238:241], v[70:73]
	v_mfma_f32_16x16x32_bf16 v[66:69], v[154:157], v[238:241], v[66:69]
	v_mfma_f32_16x16x32_bf16 v[110:113], v[150:153], v[198:201], v[110:113]
	v_mfma_f32_16x16x32_bf16 v[106:109], v[158:161], v[198:201], v[106:109]
	v_mfma_f32_16x16x32_bf16 v[102:105], v[150:153], v[216:219], v[102:105]
	v_mfma_f32_16x16x32_bf16 v[98:101], v[158:161], v[216:219], v[98:101]
	v_mfma_f32_16x16x32_bf16 v[78:81], v[150:153], v[234:237], v[78:81]
	v_mfma_f32_16x16x32_bf16 v[74:77], v[158:161], v[234:237], v[74:77]
	v_mfma_f32_16x16x32_bf16 v[70:73], v[150:153], v[242:245], v[70:73]
	v_mfma_f32_16x16x32_bf16 v[66:69], v[158:161], v[242:245], v[66:69]
	s_setprio 0
	s_barrier
	s_add_i32 s64, s86, s67
	v_lshl_add_u64 v[202:203], v[202:203], 0, s[22:23]
	s_mov_b32 m0, s64
	ds_read_b128 v[184:187], v210 offset:49152
	ds_read_b128 v[198:201], v210 offset:50176
	ds_read_b128 v[212:215], v210 offset:51200
	ds_read_b128 v[216:219], v210 offset:52224
	ds_read_b128 v[220:223], v210 offset:53248
	ds_read_b128 v[234:237], v210 offset:54272
	ds_read_b128 v[238:241], v210 offset:55296
	ds_read_b128 v[242:245], v210 offset:56320
	global_load_lds_dwordx4 v[202:203], off
	s_add_i32 m0, s64, 0x2000
	s_add_u32 s62, s62, 0x40080
	v_lshl_add_u64 v[202:203], v[246:247], 0, s[22:23]
	s_addc_u32 s63, s63, 0
	s_add_i32 s64, s87, s67
	global_load_lds_dwordx4 v[202:203], off
	v_lshl_add_u64 v[202:203], s[62:63], 0, v[166:167]
	s_mov_b32 m0, s64
	s_nop 0
	global_load_lds_dwordx4 v[202:203], off
	v_lshl_add_u64 v[202:203], s[62:63], 0, v[170:171]
	s_add_i32 m0, s64, 0x2000
	s_nop 0
	global_load_lds_dwordx4 v[202:203], off
	v_lshl_add_u64 v[202:203], v[248:249], 0, s[22:23]
	s_mov_b32 m0, s78
	s_nop 0
	global_load_lds_dwordx4 v[202:203], off
	v_lshl_add_u64 v[202:203], v[250:251], 0, s[22:23]
	s_mov_b32 m0, s79
	s_nop 0
	global_load_lds_dwordx4 v[202:203], off
	s_waitcnt vmcnt(8)
	s_waitcnt lgkmcnt(0)
	s_barrier
	s_setprio 1
	s_waitcnt lgkmcnt(0)
	v_mfma_f32_16x16x32_bf16 v[62:65], v[130:133], v[184:187], v[62:65]
	v_mfma_f32_16x16x32_bf16 v[58:61], v[138:141], v[184:187], v[58:61]
	v_mfma_f32_16x16x32_bf16 v[54:57], v[130:133], v[212:215], v[54:57]
	v_mfma_f32_16x16x32_bf16 v[50:53], v[138:141], v[212:215], v[50:53]
	v_mfma_f32_16x16x32_bf16 v[30:33], v[130:133], v[220:223], v[30:33]
	v_mfma_f32_16x16x32_bf16 v[26:29], v[138:141], v[220:223], v[26:29]
	v_mfma_f32_16x16x32_bf16 v[22:25], v[130:133], v[238:241], v[22:25]
	v_mfma_f32_16x16x32_bf16 v[18:21], v[138:141], v[238:241], v[18:21]
	v_mfma_f32_16x16x32_bf16 v[62:65], v[134:137], v[198:201], v[62:65]
	v_mfma_f32_16x16x32_bf16 v[58:61], v[142:145], v[198:201], v[58:61]
	v_mfma_f32_16x16x32_bf16 v[54:57], v[134:137], v[216:219], v[54:57]
	v_mfma_f32_16x16x32_bf16 v[50:53], v[142:145], v[216:219], v[50:53]
	v_mfma_f32_16x16x32_bf16 v[30:33], v[134:137], v[234:237], v[30:33]
	v_mfma_f32_16x16x32_bf16 v[26:29], v[142:145], v[234:237], v[26:29]
	v_mfma_f32_16x16x32_bf16 v[22:25], v[134:137], v[242:245], v[22:25]
	v_mfma_f32_16x16x32_bf16 v[18:21], v[142:145], v[242:245], v[18:21]
	v_mfma_f32_16x16x32_bf16 v[46:49], v[146:149], v[184:187], v[46:49]
	v_mfma_f32_16x16x32_bf16 v[42:45], v[154:157], v[184:187], v[42:45]
	v_mfma_f32_16x16x32_bf16 v[38:41], v[146:149], v[212:215], v[38:41]
	v_mfma_f32_16x16x32_bf16 v[34:37], v[154:157], v[212:215], v[34:37]
	v_mfma_f32_16x16x32_bf16 v[14:17], v[146:149], v[220:223], v[14:17]
	v_mfma_f32_16x16x32_bf16 v[10:13], v[154:157], v[220:223], v[10:13]
	v_mfma_f32_16x16x32_bf16 v[6:9], v[146:149], v[238:241], v[6:9]
	v_mfma_f32_16x16x32_bf16 v[2:5], v[154:157], v[238:241], v[2:5]
	v_mfma_f32_16x16x32_bf16 v[46:49], v[150:153], v[198:201], v[46:49]
	v_mfma_f32_16x16x32_bf16 v[42:45], v[158:161], v[198:201], v[42:45]
	v_mfma_f32_16x16x32_bf16 v[38:41], v[150:153], v[216:219], v[38:41]
	v_mfma_f32_16x16x32_bf16 v[34:37], v[158:161], v[216:219], v[34:37]
	v_mfma_f32_16x16x32_bf16 v[14:17], v[150:153], v[234:237], v[14:17]
	v_mfma_f32_16x16x32_bf16 v[10:13], v[158:161], v[234:237], v[10:13]
	v_mfma_f32_16x16x32_bf16 v[6:9], v[150:153], v[242:245], v[6:9]
	v_mfma_f32_16x16x32_bf16 v[2:5], v[158:161], v[242:245], v[2:5]
	s_setprio 0
	s_barrier
	s_add_i32 s85, s85, 2
	s_add_u32 s36, s36, 0x100
	s_addc_u32 s37, s37, 0
	s_add_u32 s74, s74, 0x100
	s_addc_u32 s84, s84, 0
	s_cmp_gt_u32 s85, 13
	s_cbranch_scc0 .LBB0_673
	s_and_b64 vcc, exec, s[52:53]
	s_cbranch_vccz .LBB0_676
	s_barrier

.LBB0_699:
	s_add_u32 s50, s48, 0xfffc0080
	s_addc_u32 s51, s49, -1
	s_add_i32 s79, 0, 0x10000
	s_cmp_eq_u32 s78, 12
	s_cselect_b32 s53, s41, s51
	s_cselect_b32 s52, s71, s50
	v_add_u32_e32 v132, s79, v138
	s_cselect_b32 s51, s39, s75
	s_cselect_b32 s50, s73, s74
	s_add_i32 s84, 0, 0x14000
	ds_read_b128 v[142:145], v132
	ds_read_b128 v[146:149], v132 offset:1024
	ds_read_b128 v[150:153], v132 offset:2048
	ds_read_b128 v[154:157], v132 offset:3072
	v_add_u32_e32 v132, s84, v138
	ds_read_b128 v[158:161], v132
	ds_read_b128 v[172:175], v132 offset:1024
	ds_read_b128 v[180:183], v132 offset:2048
	ds_read_b128 v[184:187], v132 offset:3072
	v_lshl_add_u64 v[132:133], s[48:49], 0, v[0:1]
	s_add_i32 m0, s47, 0xc000
	ds_read_b128 v[196:199], v140
	ds_read_b128 v[200:203], v140 offset:1024
	ds_read_b128 v[204:207], v140 offset:2048
	ds_read_b128 v[208:211], v140 offset:3072
	ds_read_b128 v[212:215], v140 offset:4096
	ds_read_b128 v[216:219], v140 offset:5120
	ds_read_b128 v[220:223], v140 offset:6144
	ds_read_b128 v[234:237], v140 offset:7168
	global_load_lds_dwordx4 v[132:133], off
	v_lshl_add_u64 v[132:133], s[48:49], 0, v[130:131]
	s_add_i32 m0, s47, 0xe000
	s_nop 0
	global_load_lds_dwordx4 v[132:133], off
	s_waitcnt vmcnt(8)
	s_waitcnt lgkmcnt(0)
	s_barrier
	s_setprio 1
	s_waitcnt lgkmcnt(0)
	v_mfma_f32_16x16x32_bf16 v[126:129], v[142:145], v[196:199], v[126:129]
	v_mfma_f32_16x16x32_bf16 v[122:125], v[150:153], v[196:199], v[122:125]
	v_mfma_f32_16x16x32_bf16 v[118:121], v[142:145], v[204:207], v[118:121]
	v_mfma_f32_16x16x32_bf16 v[110:113], v[150:153], v[204:207], v[110:113]
	v_mfma_f32_16x16x32_bf16 v[102:105], v[142:145], v[212:215], v[102:105]
	v_mfma_f32_16x16x32_bf16 v[94:97], v[150:153], v[212:215], v[94:97]
	v_mfma_f32_16x16x32_bf16 v[86:89], v[142:145], v[220:223], v[86:89]
	v_mfma_f32_16x16x32_bf16 v[78:81], v[150:153], v[220:223], v[78:81]
	v_mfma_f32_16x16x32_bf16 v[126:129], v[146:149], v[200:203], v[126:129]
	v_mfma_f32_16x16x32_bf16 v[122:125], v[154:157], v[200:203], v[122:125]
	v_mfma_f32_16x16x32_bf16 v[118:121], v[146:149], v[208:211], v[118:121]
	v_mfma_f32_16x16x32_bf16 v[110:113], v[154:157], v[208:211], v[110:113]
	v_mfma_f32_16x16x32_bf16 v[102:105], v[146:149], v[216:219], v[102:105]
	v_mfma_f32_16x16x32_bf16 v[94:97], v[154:157], v[216:219], v[94:97]
	v_mfma_f32_16x16x32_bf16 v[86:89], v[146:149], v[234:237], v[86:89]
	v_mfma_f32_16x16x32_bf16 v[78:81], v[154:157], v[234:237], v[78:81]
	v_mfma_f32_16x16x32_bf16 v[114:117], v[158:161], v[196:199], v[114:117]
	v_mfma_f32_16x16x32_bf16 v[106:109], v[180:183], v[196:199], v[106:109]
	v_mfma_f32_16x16x32_bf16 v[98:101], v[158:161], v[204:207], v[98:101]
	v_mfma_f32_16x16x32_bf16 v[90:93], v[180:183], v[204:207], v[90:93]
	v_mfma_f32_16x16x32_bf16 v[82:85], v[158:161], v[212:215], v[82:85]
	v_mfma_f32_16x16x32_bf16 v[74:77], v[180:183], v[212:215], v[74:77]
	v_mfma_f32_16x16x32_bf16 v[70:73], v[158:161], v[220:223], v[70:73]
	v_mfma_f32_16x16x32_bf16 v[66:69], v[180:183], v[220:223], v[66:69]
	v_mfma_f32_16x16x32_bf16 v[114:117], v[172:175], v[200:203], v[114:117]
	v_mfma_f32_16x16x32_bf16 v[106:109], v[184:187], v[200:203], v[106:109]
	v_mfma_f32_16x16x32_bf16 v[98:101], v[172:175], v[208:211], v[98:101]
	v_mfma_f32_16x16x32_bf16 v[90:93], v[184:187], v[208:211], v[90:93]
	v_mfma_f32_16x16x32_bf16 v[82:85], v[172:175], v[216:219], v[82:85]
	v_mfma_f32_16x16x32_bf16 v[74:77], v[184:187], v[216:219], v[74:77]
	v_mfma_f32_16x16x32_bf16 v[70:73], v[172:175], v[234:237], v[70:73]
	v_mfma_f32_16x16x32_bf16 v[66:69], v[184:187], v[234:237], v[66:69]
	s_setprio 0
	s_barrier
	s_add_i32 s79, s79, s63
	v_lshl_add_u64 v[132:133], s[50:51], 0, v[166:167]
	s_mov_b32 m0, s79
	ds_read_b128 v[196:199], v140 offset:16384
	ds_read_b128 v[200:203], v140 offset:17408
	ds_read_b128 v[204:207], v140 offset:18432
	ds_read_b128 v[208:211], v140 offset:19456
	ds_read_b128 v[212:215], v140 offset:20480
	ds_read_b128 v[216:219], v140 offset:21504
	ds_read_b128 v[220:223], v140 offset:22528
	ds_read_b128 v[234:237], v140 offset:23552
	global_load_lds_dwordx4 v[132:133], off
	s_add_i32 m0, s79, 0x2000
	s_add_u32 s82, s50, 0x40000
	v_lshl_add_u64 v[188:189], s[50:51], 0, v[170:171]
	s_addc_u32 s83, s51, 0
	s_add_i32 s79, s84, s63
	global_load_lds_dwordx4 v[188:189], off
	v_lshl_add_u64 v[230:231], s[82:83], 0, v[166:167]
	s_mov_b32 m0, s79
	v_lshl_add_u64 v[238:239], s[52:53], 0, v[168:169]
	global_load_lds_dwordx4 v[230:231], off
	v_lshl_add_u64 v[230:231], s[82:83], 0, v[170:171]
	s_add_i32 m0, s79, 0x2000
	s_nop 0
	global_load_lds_dwordx4 v[230:231], off
	v_lshl_add_u64 v[230:231], s[52:53], 0, v[164:165]
	s_mov_b32 m0, s47
	s_nop 0
	global_load_lds_dwordx4 v[230:231], off
	s_mov_b32 m0, s64
	s_nop 0
	global_load_lds_dwordx4 v[238:239], off
	s_waitcnt vmcnt(8)
	s_waitcnt lgkmcnt(0)
	s_barrier
	s_setprio 1
	s_waitcnt lgkmcnt(0)
	v_mfma_f32_16x16x32_bf16 v[62:65], v[142:145], v[196:199], v[62:65]
	v_mfma_f32_16x16x32_bf16 v[58:61], v[150:153], v[196:199], v[58:61]
	v_mfma_f32_16x16x32_bf16 v[54:57], v[142:145], v[204:207], v[54:57]
	v_mfma_f32_16x16x32_bf16 v[46:49], v[150:153], v[204:207], v[46:49]
	v_mfma_f32_16x16x32_bf16 v[38:41], v[142:145], v[212:215], v[38:41]
	v_mfma_f32_16x16x32_bf16 v[30:33], v[150:153], v[212:215], v[30:33]
	v_mfma_f32_16x16x32_bf16 v[22:25], v[142:145], v[220:223], v[22:25]
	v_mfma_f32_16x16x32_bf16 v[14:17], v[150:153], v[220:223], v[14:17]
	v_mfma_f32_16x16x32_bf16 v[62:65], v[146:149], v[200:203], v[62:65]
	v_mfma_f32_16x16x32_bf16 v[58:61], v[154:157], v[200:203], v[58:61]
	v_mfma_f32_16x16x32_bf16 v[54:57], v[146:149], v[208:211], v[54:57]
	v_mfma_f32_16x16x32_bf16 v[46:49], v[154:157], v[208:211], v[46:49]
	v_mfma_f32_16x16x32_bf16 v[38:41], v[146:149], v[216:219], v[38:41]
	v_mfma_f32_16x16x32_bf16 v[30:33], v[154:157], v[216:219], v[30:33]
	v_mfma_f32_16x16x32_bf16 v[22:25], v[146:149], v[234:237], v[22:25]
	v_mfma_f32_16x16x32_bf16 v[14:17], v[154:157], v[234:237], v[14:17]
	v_mfma_f32_16x16x32_bf16 v[50:53], v[158:161], v[196:199], v[50:53]
	v_mfma_f32_16x16x32_bf16 v[42:45], v[180:183], v[196:199], v[42:45]
	v_mfma_f32_16x16x32_bf16 v[34:37], v[158:161], v[204:207], v[34:37]
	v_mfma_f32_16x16x32_bf16 v[26:29], v[180:183], v[204:207], v[26:29]
	v_mfma_f32_16x16x32_bf16 v[18:21], v[158:161], v[212:215], v[18:21]
	v_mfma_f32_16x16x32_bf16 v[10:13], v[180:183], v[212:215], v[10:13]
	v_mfma_f32_16x16x32_bf16 v[6:9], v[158:161], v[220:223], v[6:9]
	v_mfma_f32_16x16x32_bf16 v[2:5], v[180:183], v[220:223], v[2:5]
	v_mfma_f32_16x16x32_bf16 v[50:53], v[172:175], v[200:203], v[50:53]
	v_mfma_f32_16x16x32_bf16 v[42:45], v[184:187], v[200:203], v[42:45]
	v_mfma_f32_16x16x32_bf16 v[34:37], v[172:175], v[208:211], v[34:37]
	v_mfma_f32_16x16x32_bf16 v[26:29], v[184:187], v[208:211], v[26:29]
	v_mfma_f32_16x16x32_bf16 v[18:21], v[172:175], v[216:219], v[18:21]
	v_mfma_f32_16x16x32_bf16 v[10:13], v[184:187], v[216:219], v[10:13]
	v_mfma_f32_16x16x32_bf16 v[6:9], v[172:175], v[234:237], v[6:9]
	v_mfma_f32_16x16x32_bf16 v[2:5], v[184:187], v[234:237], v[2:5]
	s_setprio 0
	s_barrier
	s_add_i32 s79, 0, 0x18000
	v_add_u32_e32 v141, s79, v138
	s_add_i32 s82, 0, 0x1c000
	ds_read_b128 v[142:145], v141
	ds_read_b128 v[146:149], v141 offset:1024
	ds_read_b128 v[150:153], v141 offset:2048
	ds_read_b128 v[154:157], v141 offset:3072
	v_add_u32_e32 v141, s82, v138
	ds_read_b128 v[158:161], v141
	ds_read_b128 v[172:175], v141 offset:1024
	ds_read_b128 v[180:183], v141 offset:2048
	ds_read_b128 v[184:187], v141 offset:3072
	s_add_u32 s52, s52, 0x40000
	s_addc_u32 s53, s53, 0
	s_mov_b32 m0, s65
	v_lshl_add_u64 v[240:241], s[52:53], 0, v[164:165]
	ds_read_b128 v[196:199], v140 offset:32768
	ds_read_b128 v[200:203], v140 offset:33792
	ds_read_b128 v[204:207], v140 offset:34816
	ds_read_b128 v[208:211], v140 offset:35840
	ds_read_b128 v[212:215], v140 offset:36864
	ds_read_b128 v[216:219], v140 offset:37888
	ds_read_b128 v[220:223], v140 offset:38912
	ds_read_b128 v[234:237], v140 offset:39936
	global_load_lds_dwordx4 v[240:241], off
	v_lshl_add_u64 v[240:241], s[52:53], 0, v[168:169]
	s_mov_b32 m0, s66
	s_nop 0
	global_load_lds_dwordx4 v[240:241], off
	s_waitcnt vmcnt(8)
	s_waitcnt lgkmcnt(0)
	s_barrier
	s_setprio 1
	s_waitcnt lgkmcnt(0)
	v_mfma_f32_16x16x32_bf16 v[126:129], v[142:145], v[196:199], v[126:129]
	v_mfma_f32_16x16x32_bf16 v[122:125], v[150:153], v[196:199], v[122:125]
	v_mfma_f32_16x16x32_bf16 v[118:121], v[142:145], v[204:207], v[118:121]
	v_mfma_f32_16x16x32_bf16 v[110:113], v[150:153], v[204:207], v[110:113]
	v_mfma_f32_16x16x32_bf16 v[102:105], v[142:145], v[212:215], v[102:105]
	v_mfma_f32_16x16x32_bf16 v[94:97], v[150:153], v[212:215], v[94:97]
	v_mfma_f32_16x16x32_bf16 v[86:89], v[142:145], v[220:223], v[86:89]
	v_mfma_f32_16x16x32_bf16 v[78:81], v[150:153], v[220:223], v[78:81]
	v_mfma_f32_16x16x32_bf16 v[126:129], v[146:149], v[200:203], v[126:129]
	v_mfma_f32_16x16x32_bf16 v[122:125], v[154:157], v[200:203], v[122:125]
	v_mfma_f32_16x16x32_bf16 v[118:121], v[146:149], v[208:211], v[118:121]
	v_mfma_f32_16x16x32_bf16 v[110:113], v[154:157], v[208:211], v[110:113]
	v_mfma_f32_16x16x32_bf16 v[102:105], v[146:149], v[216:219], v[102:105]
	v_mfma_f32_16x16x32_bf16 v[94:97], v[154:157], v[216:219], v[94:97]
	v_mfma_f32_16x16x32_bf16 v[86:89], v[146:149], v[234:237], v[86:89]
	v_mfma_f32_16x16x32_bf16 v[78:81], v[154:157], v[234:237], v[78:81]
	v_mfma_f32_16x16x32_bf16 v[114:117], v[158:161], v[196:199], v[114:117]
	v_mfma_f32_16x16x32_bf16 v[106:109], v[180:183], v[196:199], v[106:109]
	v_mfma_f32_16x16x32_bf16 v[98:101], v[158:161], v[204:207], v[98:101]
	v_mfma_f32_16x16x32_bf16 v[90:93], v[180:183], v[204:207], v[90:93]
	v_mfma_f32_16x16x32_bf16 v[82:85], v[158:161], v[212:215], v[82:85]
	v_mfma_f32_16x16x32_bf16 v[74:77], v[180:183], v[212:215], v[74:77]
	v_mfma_f32_16x16x32_bf16 v[70:73], v[158:161], v[220:223], v[70:73]
	v_mfma_f32_16x16x32_bf16 v[66:69], v[180:183], v[220:223], v[66:69]
	v_mfma_f32_16x16x32_bf16 v[114:117], v[172:175], v[200:203], v[114:117]
	v_mfma_f32_16x16x32_bf16 v[106:109], v[184:187], v[200:203], v[106:109]
	v_mfma_f32_16x16x32_bf16 v[98:101], v[172:175], v[208:211], v[98:101]
	v_mfma_f32_16x16x32_bf16 v[90:93], v[184:187], v[208:211], v[90:93]
	v_mfma_f32_16x16x32_bf16 v[82:85], v[172:175], v[216:219], v[82:85]
	v_mfma_f32_16x16x32_bf16 v[74:77], v[184:187], v[216:219], v[74:77]
	v_mfma_f32_16x16x32_bf16 v[70:73], v[172:175], v[234:237], v[70:73]
	v_mfma_f32_16x16x32_bf16 v[66:69], v[184:187], v[234:237], v[66:69]
	s_setprio 0
	s_barrier
	s_add_i32 s52, s79, s63
	v_lshl_add_u64 v[132:133], v[132:133], 0, s[22:23]
	s_mov_b32 m0, s52
	ds_read_b128 v[196:199], v140 offset:49152
	ds_read_b128 v[200:203], v140 offset:50176
	ds_read_b128 v[204:207], v140 offset:51200
	ds_read_b128 v[208:211], v140 offset:52224
	ds_read_b128 v[212:215], v140 offset:53248
	ds_read_b128 v[216:219], v140 offset:54272
	ds_read_b128 v[220:223], v140 offset:55296
	ds_read_b128 v[234:237], v140 offset:56320
	global_load_lds_dwordx4 v[132:133], off
	s_add_i32 m0, s52, 0x2000
	s_add_u32 s50, s50, 0x40080
	v_lshl_add_u64 v[132:133], v[188:189], 0, s[22:23]
	s_addc_u32 s51, s51, 0
	s_add_i32 s52, s82, s63
	global_load_lds_dwordx4 v[132:133], off
	v_lshl_add_u64 v[132:133], s[50:51], 0, v[166:167]
	s_mov_b32 m0, s52
	s_nop 0
	global_load_lds_dwordx4 v[132:133], off
	v_lshl_add_u64 v[132:133], s[50:51], 0, v[170:171]
	s_add_i32 m0, s52, 0x2000
	s_nop 0
	global_load_lds_dwordx4 v[132:133], off
	v_lshl_add_u64 v[132:133], v[230:231], 0, s[22:23]
	s_mov_b32 m0, s67
	s_nop 0
	global_load_lds_dwordx4 v[132:133], off
	v_lshl_add_u64 v[132:133], v[238:239], 0, s[22:23]
	s_mov_b32 m0, s68
	s_nop 0
	global_load_lds_dwordx4 v[132:133], off
	s_waitcnt vmcnt(8)
	s_waitcnt lgkmcnt(0)
	s_barrier
	s_setprio 1
	s_waitcnt lgkmcnt(0)
	v_mfma_f32_16x16x32_bf16 v[62:65], v[142:145], v[196:199], v[62:65]
	v_mfma_f32_16x16x32_bf16 v[58:61], v[150:153], v[196:199], v[58:61]
	v_mfma_f32_16x16x32_bf16 v[54:57], v[142:145], v[204:207], v[54:57]
	v_mfma_f32_16x16x32_bf16 v[46:49], v[150:153], v[204:207], v[46:49]
	v_mfma_f32_16x16x32_bf16 v[38:41], v[142:145], v[212:215], v[38:41]
	v_mfma_f32_16x16x32_bf16 v[30:33], v[150:153], v[212:215], v[30:33]
	v_mfma_f32_16x16x32_bf16 v[22:25], v[142:145], v[220:223], v[22:25]
	v_mfma_f32_16x16x32_bf16 v[14:17], v[150:153], v[220:223], v[14:17]
	v_mfma_f32_16x16x32_bf16 v[62:65], v[146:149], v[200:203], v[62:65]
	v_mfma_f32_16x16x32_bf16 v[58:61], v[154:157], v[200:203], v[58:61]
	v_mfma_f32_16x16x32_bf16 v[54:57], v[146:149], v[208:211], v[54:57]
	v_mfma_f32_16x16x32_bf16 v[46:49], v[154:157], v[208:211], v[46:49]
	v_mfma_f32_16x16x32_bf16 v[38:41], v[146:149], v[216:219], v[38:41]
	v_mfma_f32_16x16x32_bf16 v[30:33], v[154:157], v[216:219], v[30:33]
	v_mfma_f32_16x16x32_bf16 v[22:25], v[146:149], v[234:237], v[22:25]
	v_mfma_f32_16x16x32_bf16 v[14:17], v[154:157], v[234:237], v[14:17]
	v_mfma_f32_16x16x32_bf16 v[50:53], v[158:161], v[196:199], v[50:53]
	v_mfma_f32_16x16x32_bf16 v[42:45], v[180:183], v[196:199], v[42:45]
	v_mfma_f32_16x16x32_bf16 v[34:37], v[158:161], v[204:207], v[34:37]
	v_mfma_f32_16x16x32_bf16 v[26:29], v[180:183], v[204:207], v[26:29]
	v_mfma_f32_16x16x32_bf16 v[18:21], v[158:161], v[212:215], v[18:21]
	v_mfma_f32_16x16x32_bf16 v[10:13], v[180:183], v[212:215], v[10:13]
	v_mfma_f32_16x16x32_bf16 v[6:9], v[158:161], v[220:223], v[6:9]
	v_mfma_f32_16x16x32_bf16 v[2:5], v[180:183], v[220:223], v[2:5]
	v_mfma_f32_16x16x32_bf16 v[50:53], v[172:175], v[200:203], v[50:53]
	v_mfma_f32_16x16x32_bf16 v[42:45], v[184:187], v[200:203], v[42:45]
	v_mfma_f32_16x16x32_bf16 v[34:37], v[172:175], v[208:211], v[34:37]
	v_mfma_f32_16x16x32_bf16 v[26:29], v[184:187], v[208:211], v[26:29]
	v_mfma_f32_16x16x32_bf16 v[18:21], v[172:175], v[216:219], v[18:21]
	v_mfma_f32_16x16x32_bf16 v[10:13], v[184:187], v[216:219], v[10:13]
	v_mfma_f32_16x16x32_bf16 v[6:9], v[172:175], v[234:237], v[6:9]
	v_mfma_f32_16x16x32_bf16 v[2:5], v[184:187], v[234:237], v[2:5]
	s_setprio 0
	s_barrier
	s_add_i32 s78, s78, 2
	s_add_u32 s48, s48, 0x100
	s_addc_u32 s49, s49, 0
	s_add_u32 s74, s74, 0x100
	s_addc_u32 s75, s75, 0
	s_cmp_gt_u32 s78, 13
	s_cbranch_scc0 .LBB0_699
	v_lshl_add_u32 v142, s46, 8, v137
	v_lshl_or_b32 v132, s70, 8, v139
	v_ashrrev_i32_e32 v143, 31, v142
	v_ashrrev_i32_e32 v133, 31, v132
	v_lshlrev_b64 v[144:145], 10, v[142:143]
	v_lshl_add_u64 v[144:145], s[26:27], 0, v[144:145]
	v_lshlrev_b64 v[146:147], 1, v[132:133]
	v_lshl_add_u64 v[132:133], v[144:145], 0, v[146:147]
	v_pk_add_f32 v[128:129], v[128:129], 0 op_sel_hi:[1,0]
	v_pk_add_f32 v[126:127], v[126:127], 0 op_sel_hi:[1,0]
	v_pk_add_f32 v[144:145], v[124:125], 0 op_sel_hi:[1,0]
	v_pk_add_f32 v[124:125], v[122:123], 0 op_sel_hi:[1,0]
	v_cvt_pk_bf16_f32 v122, v126, v127
	v_cvt_pk_bf16_f32 v123, v128, v129
	v_cvt_pk_bf16_f32 v124, v124, v125
	v_cvt_pk_bf16_f32 v125, v144, v145
	global_store_dwordx4 v[132:133], v[122:125], off
	v_pk_add_f32 v[116:117], v[116:117], 0 op_sel_hi:[1,0]
	v_pk_add_f32 v[114:115], v[114:115], 0 op_sel_hi:[1,0]
	v_pk_add_f32 v[122:123], v[108:109], 0 op_sel_hi:[1,0]
	v_pk_add_f32 v[108:109], v[106:107], 0 op_sel_hi:[1,0]
	v_cvt_pk_bf16_f32 v106, v114, v115
	v_cvt_pk_bf16_f32 v107, v116, v117
	v_cvt_pk_bf16_f32 v108, v108, v109
	v_cvt_pk_bf16_f32 v109, v122, v123
	global_store_dwordx4 v[132:133], v[106:109], off offset:256
	v_pk_add_f32 v[112:113], v[112:113], 0 op_sel_hi:[1,0]
	v_pk_add_f32 v[110:111], v[110:111], 0 op_sel_hi:[1,0]
	v_or_b32_e32 v106, 16, v142
	v_ashrrev_i32_e32 v107, 31, v106
	v_lshlrev_b64 v[106:107], 10, v[106:107]
	v_lshl_add_u64 v[106:107], s[26:27], 0, v[106:107]
	v_lshl_add_u64 v[114:115], v[106:107], 0, v[146:147]
	v_pk_add_f32 v[108:109], v[120:121], 0 op_sel_hi:[1,0]
	v_pk_add_f32 v[106:107], v[118:119], 0 op_sel_hi:[1,0]
	v_pk_add_f32 v[100:101], v[100:101], 0 op_sel_hi:[1,0]
	v_cvt_pk_bf16_f32 v106, v106, v107
	v_cvt_pk_bf16_f32 v107, v108, v109
	v_cvt_pk_bf16_f32 v108, v110, v111
	v_cvt_pk_bf16_f32 v109, v112, v113
	global_store_dwordx4 v[114:115], v[106:109], off
	v_pk_add_f32 v[98:99], v[98:99], 0 op_sel_hi:[1,0]
	v_pk_add_f32 v[96:97], v[96:97], 0 op_sel_hi:[1,0]
	v_pk_add_f32 v[106:107], v[92:93], 0 op_sel_hi:[1,0]
	v_pk_add_f32 v[92:93], v[90:91], 0 op_sel_hi:[1,0]
	v_cvt_pk_bf16_f32 v90, v98, v99
	v_cvt_pk_bf16_f32 v91, v100, v101
	v_cvt_pk_bf16_f32 v92, v92, v93
	v_cvt_pk_bf16_f32 v93, v106, v107
	global_store_dwordx4 v[114:115], v[90:93], off offset:256
	v_pk_add_f32 v[94:95], v[94:95], 0 op_sel_hi:[1,0]
	v_pk_add_f32 v[84:85], v[84:85], 0 op_sel_hi:[1,0]
	v_or_b32_e32 v90, 32, v142
	v_ashrrev_i32_e32 v91, 31, v90
	v_lshlrev_b64 v[90:91], 10, v[90:91]
	v_lshl_add_u64 v[90:91], s[26:27], 0, v[90:91]
	v_lshl_add_u64 v[98:99], v[90:91], 0, v[146:147]
	v_pk_add_f32 v[92:93], v[104:105], 0 op_sel_hi:[1,0]
	v_pk_add_f32 v[90:91], v[102:103], 0 op_sel_hi:[1,0]
	v_pk_add_f32 v[82:83], v[82:83], 0 op_sel_hi:[1,0]
	v_cvt_pk_bf16_f32 v90, v90, v91
	v_cvt_pk_bf16_f32 v91, v92, v93
	v_cvt_pk_bf16_f32 v92, v94, v95
	v_cvt_pk_bf16_f32 v93, v96, v97
	global_store_dwordx4 v[98:99], v[90:93], off
	v_pk_add_f32 v[80:81], v[80:81], 0 op_sel_hi:[1,0]
	v_pk_add_f32 v[78:79], v[78:79], 0 op_sel_hi:[1,0]
	v_pk_add_f32 v[90:91], v[76:77], 0 op_sel_hi:[1,0]
	v_pk_add_f32 v[76:77], v[74:75], 0 op_sel_hi:[1,0]
	v_cvt_pk_bf16_f32 v74, v82, v83
	v_cvt_pk_bf16_f32 v75, v84, v85
	v_cvt_pk_bf16_f32 v76, v76, v77
	v_cvt_pk_bf16_f32 v77, v90, v91
	global_store_dwordx4 v[98:99], v[74:77], off offset:256
	v_pk_add_f32 v[72:73], v[72:73], 0 op_sel_hi:[1,0]
	v_pk_add_f32 v[70:71], v[70:71], 0 op_sel_hi:[1,0]
	v_or_b32_e32 v74, 48, v142
	v_ashrrev_i32_e32 v75, 31, v74
	v_lshlrev_b64 v[74:75], 10, v[74:75]
	v_lshl_add_u64 v[74:75], s[26:27], 0, v[74:75]
	v_lshl_add_u64 v[82:83], v[74:75], 0, v[146:147]
	v_pk_add_f32 v[76:77], v[88:89], 0 op_sel_hi:[1,0]
	v_pk_add_f32 v[74:75], v[86:87], 0 op_sel_hi:[1,0]
	v_pk_add_f32 v[62:63], v[62:63], 0 op_sel_hi:[1,0]
	v_cvt_pk_bf16_f32 v74, v74, v75
	v_cvt_pk_bf16_f32 v75, v76, v77
	v_cvt_pk_bf16_f32 v76, v78, v79
	v_cvt_pk_bf16_f32 v77, v80, v81
	global_store_dwordx4 v[82:83], v[74:77], off
	s_mov_b32 s39, 0x20000
	v_pk_add_f32 v[64:65], v[64:65], 0 op_sel_hi:[1,0]
	v_pk_add_f32 v[74:75], v[68:69], 0 op_sel_hi:[1,0]
	v_pk_add_f32 v[68:69], v[66:67], 0 op_sel_hi:[1,0]
	v_cvt_pk_bf16_f32 v66, v70, v71
	v_cvt_pk_bf16_f32 v67, v72, v73
	v_cvt_pk_bf16_f32 v68, v68, v69
	v_cvt_pk_bf16_f32 v69, v74, v75
	global_store_dwordx4 v[82:83], v[66:69], off offset:256
	s_mov_b64 s[48:49], 0x20000
	v_pk_add_f32 v[52:53], v[52:53], 0 op_sel_hi:[1,0]
	v_pk_add_f32 v[68:69], v[60:61], 0 op_sel_hi:[1,0]
	v_pk_add_f32 v[60:61], v[58:59], 0 op_sel_hi:[1,0]
	v_cvt_pk_bf16_f32 v58, v62, v63
	v_add_co_u32_e32 v62, vcc, s39, v132
	v_cvt_pk_bf16_f32 v59, v64, v65
	v_cvt_pk_bf16_f32 v60, v60, v61
	v_cvt_pk_bf16_f32 v61, v68, v69
	v_addc_co_u32_e32 v63, vcc, 0, v133, vcc
	global_store_dwordx4 v[62:63], v[58:61], off
	v_pk_add_f32 v[50:51], v[50:51], 0 op_sel_hi:[1,0]
	v_lshl_add_u64 v[66:67], v[132:133], 0, s[48:49]
	v_pk_add_f32 v[58:59], v[44:45], 0 op_sel_hi:[1,0]
	v_pk_add_f32 v[44:45], v[42:43], 0 op_sel_hi:[1,0]
	v_cvt_pk_bf16_f32 v42, v50, v51
	v_cvt_pk_bf16_f32 v43, v52, v53
	v_cvt_pk_bf16_f32 v44, v44, v45
	v_cvt_pk_bf16_f32 v45, v58, v59
	global_store_dwordx4 v[66:67], v[42:45], off offset:256
	v_pk_add_f32 v[46:47], v[46:47], 0 op_sel_hi:[1,0]
	s_mov_b32 s39, 0x24000
	v_pk_add_f32 v[44:45], v[56:57], 0 op_sel_hi:[1,0]
	v_pk_add_f32 v[42:43], v[54:55], 0 op_sel_hi:[1,0]
	v_pk_add_f32 v[48:49], v[48:49], 0 op_sel_hi:[1,0]
	v_cvt_pk_bf16_f32 v42, v42, v43
	v_cvt_pk_bf16_f32 v43, v44, v45
	v_cvt_pk_bf16_f32 v44, v46, v47
	v_add_co_u32_e32 v46, vcc, s39, v132
	v_cvt_pk_bf16_f32 v45, v48, v49
	s_nop 0
	v_addc_co_u32_e32 v47, vcc, 0, v133, vcc
	s_mov_b64 s[48:49], 0x24000
	global_store_dwordx4 v[46:47], v[42:45], off
	v_pk_add_f32 v[36:37], v[36:37], 0 op_sel_hi:[1,0]
	v_pk_add_f32 v[34:35], v[34:35], 0 op_sel_hi:[1,0]
	v_pk_add_f32 v[42:43], v[28:29], 0 op_sel_hi:[1,0]
	v_pk_add_f32 v[28:29], v[26:27], 0 op_sel_hi:[1,0]
	v_lshl_add_u64 v[50:51], v[132:133], 0, s[48:49]
	v_cvt_pk_bf16_f32 v26, v34, v35
	v_cvt_pk_bf16_f32 v27, v36, v37
	v_cvt_pk_bf16_f32 v28, v28, v29
	v_cvt_pk_bf16_f32 v29, v42, v43
	global_store_dwordx4 v[50:51], v[26:29], off offset:256
	v_pk_add_f32 v[30:31], v[30:31], 0 op_sel_hi:[1,0]
	s_mov_b32 s39, 0x28000
	v_pk_add_f32 v[28:29], v[40:41], 0 op_sel_hi:[1,0]
	v_pk_add_f32 v[26:27], v[38:39], 0 op_sel_hi:[1,0]
	v_pk_add_f32 v[32:33], v[32:33], 0 op_sel_hi:[1,0]
	v_cvt_pk_bf16_f32 v26, v26, v27
	v_cvt_pk_bf16_f32 v27, v28, v29
	v_cvt_pk_bf16_f32 v28, v30, v31
	v_add_co_u32_e32 v30, vcc, s39, v132
	v_cvt_pk_bf16_f32 v29, v32, v33
	s_nop 0
	v_addc_co_u32_e32 v31, vcc, 0, v133, vcc
	s_mov_b64 s[48:49], 0x28000
	global_store_dwordx4 v[30:31], v[26:29], off
	v_pk_add_f32 v[20:21], v[20:21], 0 op_sel_hi:[1,0]
	v_pk_add_f32 v[18:19], v[18:19], 0 op_sel_hi:[1,0]
	v_pk_add_f32 v[26:27], v[12:13], 0 op_sel_hi:[1,0]
	v_pk_add_f32 v[12:13], v[10:11], 0 op_sel_hi:[1,0]
	v_lshl_add_u64 v[34:35], v[132:133], 0, s[48:49]
	v_cvt_pk_bf16_f32 v10, v18, v19
	v_cvt_pk_bf16_f32 v11, v20, v21
	v_cvt_pk_bf16_f32 v12, v12, v13
	v_cvt_pk_bf16_f32 v13, v26, v27
	global_store_dwordx4 v[34:35], v[10:13], off offset:256
	v_pk_add_f32 v[14:15], v[14:15], 0 op_sel_hi:[1,0]
	s_mov_b32 s39, 0x2c000
	v_pk_add_f32 v[12:13], v[24:25], 0 op_sel_hi:[1,0]
	v_pk_add_f32 v[10:11], v[22:23], 0 op_sel_hi:[1,0]
	v_pk_add_f32 v[16:17], v[16:17], 0 op_sel_hi:[1,0]
	v_cvt_pk_bf16_f32 v10, v10, v11
	v_cvt_pk_bf16_f32 v11, v12, v13
	v_cvt_pk_bf16_f32 v12, v14, v15
	v_add_co_u32_e32 v14, vcc, s39, v132
	v_cvt_pk_bf16_f32 v13, v16, v17
	s_nop 0
	v_addc_co_u32_e32 v15, vcc, 0, v133, vcc
	s_mov_b64 s[48:49], 0x2c000
	global_store_dwordx4 v[14:15], v[10:13], off
	v_pk_add_f32 v[8:9], v[8:9], 0 op_sel_hi:[1,0]
	v_pk_add_f32 v[6:7], v[6:7], 0 op_sel_hi:[1,0]
	v_pk_add_f32 v[10:11], v[4:5], 0 op_sel_hi:[1,0]
	v_pk_add_f32 v[4:5], v[2:3], 0 op_sel_hi:[1,0]
	v_lshl_add_u64 v[18:19], v[132:133], 0, s[48:49]
	v_cvt_pk_bf16_f32 v2, v6, v7
	v_cvt_pk_bf16_f32 v3, v8, v9
	v_cvt_pk_bf16_f32 v4, v4, v5
	v_cvt_pk_bf16_f32 v5, v10, v11
	s_and_b64 vcc, exec, s[36:37]
	s_mov_b32 s70, s38
	s_mov_b32 s46, s40
	s_mov_b64 s[50:51], s[44:45]
	s_mov_b64 s[48:49], s[42:43]
	global_store_dwordx4 v[18:19], v[2:5], off offset:256
	s_cbranch_vccz .LBB0_696
	s_waitcnt vmcnt(0)
	s_cmpk_gt_u32 s57, 0xff
	s_cbranch_scc1 .LBB0_690
	s_barrier
	s_branch .LBB0_690
